# v18nt + YB stores nt in the in-projection epilogue + nt on the first layer's x residual loads (less MALL pollution by data that is evicted before reuse)
# speedup vs baseline: 1.0014x; 1.0014x over previous
; DI unsigned pk_bf16(float lo, float hi) { const f32x2 v = {lo, hi}; return __builtin_bit_cast(unsigned, __builtin_convertvector(v, bf16x2_t)); }
; DI float gelu_tanh(float x) { const float u = 1.5957691216057308f * (x + 0.044715f * x * x * x); return x * sigmoidf_(u); }
;     DI void operator()(const f32x4 (&acc)[2][2][4][2], const Unit& u, int wr, int wc, int fr, int fq) const {
;         const bool isy = u.pn < 4; bf16_t* base = isy ? YB : XR;
;         const int colo = (isy ? u.pn : u.pn - 4) * 256 + wc * 32 + 8 * fq, bcol = u.pn * 256 + wc * 32 + 8 * fq;
;         f32x4 bv[2][2];
; #pragma unroll
;         for (int bj = 0; bj < 2; ++bj)
; #pragma unroll
;             for (int n = 0; n < 2; ++n) bv[bj][n] = *(const f32x4*)(bias + bcol + bj * 128 + 4 * n);
; #pragma unroll
;         for (int ai = 0; ai < 2; ++ai)
; #pragma unroll
;             for (int m = 0; m < 4; ++m) { bf16_t* rowp = base + (size_t)(u.orow + ai * 128 + wr * 64 + m * 16 + fr) * 1024 + colo;
; #pragma unroll
;                 for (int bj = 0; bj < 2; ++bj) { f32x4 v0 = acc[ai][bj][m][0] + bv[bj][0], v1 = acc[ai][bj][m][1] + bv[bj][1];
;                     if (isy) {
; #pragma unroll
;                         for (int j = 0; j < 4; ++j) { v0[j] = gelu_tanh(v0[j]); v1[j] = gelu_tanh(v1[j]); } }
;                     u32x4 w; w.x = pk_bf16(v0[0], v0[1]); w.y = pk_bf16(v0[2], v0[3]); w.z = pk_bf16(v1[0], v1[1]); w.w = pk_bf16(v1[2], v1[3]);
;                     *(u32x4*)(rowp + bj * 128) = w; } }
.LBB0_507:
	s_and_b64 s[22:23], s[0:1], exec
	s_cselect_b32 s5, s7, s9
	s_cselect_b32 s19, s6, s8
	v_mov_b32_e32 v137, s5
	s_add_i32 s5, s4, 0xfffffc00
	s_and_b64 s[22:23], s[0:1], exec
	s_cselect_b32 s4, s4, s5
	v_or_b32_e32 v150, s4, v162
	v_add_u32_e32 v138, s43, v160
	v_mov_b32_e32 v136, s19
	v_ashrrev_i32_e32 v151, 31, v150
	v_ashrrev_i32_e32 v139, 31, v138
	v_lshl_add_u64 v[136:137], v[150:151], 1, v[136:137]
	v_lshlrev_b64 v[150:151], 11, v[138:139]
	v_cndmask_b32_e64 v139, 0, 1, s[0:1]
	v_lshl_add_u64 v[150:151], v[136:137], 0, v[150:151]
	v_cvt_pk_bf16_f32 v140, v140, v141
	v_cvt_pk_bf16_f32 v141, v142, v143
	v_cvt_pk_bf16_f32 v142, v154, v155
	v_cvt_pk_bf16_f32 v143, v152, v153
	v_pk_add_f32 v[134:135], v[134:135], v[38:39]
	v_pk_add_f32 v[132:133], v[132:133], v[36:37]
	v_pk_add_f32 v[130:131], v[130:131], v[34:35]
	v_cmp_ne_u32_e64 s[4:5], 1, v139
	s_andn2_b64 vcc, exec, s[0:1]
	v_pk_add_f32 v[128:129], v[128:129], v[32:33]
	s_cbranch_vccnz .Lw_pl0
	global_store_dwordx4 v[150:151], v[140:143], off nt
	s_branch .Lw_dn0
.Lw_pl0:
	global_store_dwordx4 v[150:151], v[140:143], off
.Lw_dn0:
	s_cbranch_vccnz .LBB0_509
	s_nop 0
	v_mul_f32_e32 v140, 0x3d372713, v128
	v_mul_f32_e32 v140, v128, v140
	v_fma_f32 v140, v128, v140, v128
	v_mul_f32_e32 v139, 0x3d372713, v132
	v_mul_f32_e32 v140, 0x3fcc422a, v140
	v_mul_f32_e32 v139, v132, v139
	v_mul_f32_e32 v140, 0xbfb8aa3b, v140
	v_fma_f32 v139, v132, v139, v132
	v_exp_f32_e32 v141, v140
	v_mul_f32_e32 v140, 0x3d372713, v133
	v_mul_f32_e32 v139, 0x3fcc422a, v139
	v_mul_f32_e32 v140, v133, v140
	v_mov_b32_e32 v142, v133
	v_mul_f32_e32 v139, 0xbfb8aa3b, v139
	v_fmac_f32_e32 v142, v142, v140
	v_exp_f32_e32 v139, v139
	v_mul_f32_e32 v140, 0x3fcc422a, v142
	v_mul_f32_e32 v140, 0xbfb8aa3b, v140
	v_exp_f32_e32 v143, v140
	v_add_f32_e32 v139, 1.0, v139
	v_rcp_f32_e32 v140, v139
	v_add_f32_e32 v139, 1.0, v141
	v_rcp_f32_e32 v142, v139
	v_add_f32_e32 v139, 1.0, v143
	v_rcp_f32_e32 v141, v139
	v_mul_f32_e32 v139, 0x3d372713, v129
	v_mul_f32_e32 v139, v129, v139
	v_mov_b32_e32 v143, v129
	v_fmac_f32_e32 v143, v143, v139
	v_mul_f32_e32 v139, 0x3fcc422a, v143
	v_mul_f32_e32 v143, 0x3d372713, v134
	v_mul_f32_e32 v143, v134, v143
	v_mul_f32_e32 v149, 0x3d372713, v130
	v_fma_f32 v143, v134, v143, v134
	v_mul_f32_e32 v149, v130, v149
	v_mul_f32_e32 v143, 0x3fcc422a, v143
	v_fma_f32 v149, v130, v149, v130
	v_mul_f32_e32 v143, 0xbfb8aa3b, v143
	v_mul_f32_e32 v149, 0x3fcc422a, v149
	v_exp_f32_e32 v143, v143
	v_mul_f32_e32 v149, 0xbfb8aa3b, v149
	v_exp_f32_e32 v149, v149
	v_mul_f32_e32 v153, 0x3d372713, v131
	v_add_f32_e32 v143, 1.0, v143
	v_rcp_f32_e32 v152, v143
	v_add_f32_e32 v143, 1.0, v149
	v_mul_f32_e32 v149, 0x3d372713, v135
	v_mul_f32_e32 v149, v135, v149
	v_fma_f32 v149, v135, v149, v135
	v_mul_f32_e32 v153, v131, v153
	v_mul_f32_e32 v149, 0x3fcc422a, v149
	v_fma_f32 v153, v131, v153, v131
	v_mul_f32_e32 v149, 0xbfb8aa3b, v149
	v_mul_f32_e32 v153, 0x3fcc422a, v153
	v_mul_f32_e32 v139, 0xbfb8aa3b, v139
	v_exp_f32_e32 v149, v149
	v_mul_f32_e32 v153, 0xbfb8aa3b, v153
	v_exp_f32_e32 v139, v139
	v_exp_f32_e32 v155, v153
	v_rcp_f32_e32 v154, v143
	v_add_f32_e32 v143, 1.0, v149
	v_add_f32_e32 v139, 1.0, v139
	v_rcp_f32_e32 v153, v143
	v_add_f32_e32 v143, 1.0, v155
	v_rcp_f32_e32 v155, v143
	v_rcp_f32_e32 v143, v139
	v_pk_mul_f32 v[134:135], v[134:135], v[152:153]
	v_pk_mul_f32 v[132:133], v[132:133], v[140:141]
	v_pk_mul_f32 v[130:131], v[130:131], v[154:155]
	v_pk_mul_f32 v[128:129], v[128:129], v[142:143]
.LBB0_509:
	v_cvt_pk_bf16_f32 v132, v132, v133
	v_cvt_pk_bf16_f32 v133, v134, v135
	v_cvt_pk_bf16_f32 v134, v128, v129
	v_cvt_pk_bf16_f32 v135, v130, v131
	v_pk_add_f32 v[126:127], v[126:127], v[54:55]
	v_pk_add_f32 v[124:125], v[124:125], v[52:53]
	v_pk_add_f32 v[122:123], v[122:123], v[50:51]
	s_and_b64 vcc, exec, s[4:5]
	v_pk_add_f32 v[128:129], v[120:121], v[48:49]
	s_cbranch_vccnz .Lw_pl1
	global_store_dwordx4 v[150:151], v[132:135], off offset:256 nt
	s_branch .Lw_dn1
.Lw_pl1:
	global_store_dwordx4 v[150:151], v[132:135], off offset:256
.Lw_dn1:
	s_cbranch_vccnz .LBB0_511
	v_mul_f32_e32 v121, 0x3d372713, v128
	v_mul_f32_e32 v121, v128, v121
	v_mul_f32_e32 v130, 0x3d372713, v125
	v_fma_f32 v121, v128, v121, v128
	v_mul_f32_e32 v130, v125, v130
	v_mov_b32_e32 v131, v125
	v_mul_f32_e32 v121, 0x3fcc422a, v121
	v_fmac_f32_e32 v131, v131, v130
	v_mul_f32_e32 v121, 0xbfb8aa3b, v121
	v_mul_f32_e32 v130, 0x3fcc422a, v131
	v_exp_f32_e32 v121, v121
	v_mul_f32_e32 v130, 0xbfb8aa3b, v130
	v_exp_f32_e32 v131, v130
	v_mul_f32_e32 v134, 0x3d372713, v127
	v_add_f32_e32 v121, 1.0, v121
	v_mul_f32_e32 v134, v127, v134
	v_rcp_f32_e32 v130, v121
	v_add_f32_e32 v121, 1.0, v131
	v_mul_f32_e32 v131, 0x3d372713, v129
	v_fma_f32 v134, v127, v134, v127
	v_mul_f32_e32 v131, v129, v131
	v_mov_b32_e32 v132, v129
	v_mul_f32_e32 v134, 0x3fcc422a, v134
	v_fmac_f32_e32 v132, v132, v131
	v_mul_f32_e32 v133, 0x3d372713, v122
	v_mul_f32_e32 v134, 0xbfb8aa3b, v134
	v_mul_f32_e32 v120, 0x3d372713, v124
	v_mul_f32_e32 v131, 0x3fcc422a, v132
	v_mul_f32_e32 v132, 0x3d372713, v126
	v_mul_f32_e32 v133, v122, v133
	v_exp_f32_e32 v135, v134
	v_mul_f32_e32 v134, 0x3d372713, v123
	v_mul_f32_e32 v120, v124, v120
	v_mul_f32_e32 v132, v126, v132
	v_fma_f32 v133, v122, v133, v122
	v_mul_f32_e32 v134, v123, v134
	v_fma_f32 v120, v124, v120, v124
	v_fma_f32 v132, v126, v132, v126
	v_mul_f32_e32 v133, 0x3fcc422a, v133
	v_fma_f32 v134, v123, v134, v123
	v_mul_f32_e32 v120, 0x3fcc422a, v120
	v_mul_f32_e32 v132, 0x3fcc422a, v132
	v_mul_f32_e32 v133, 0xbfb8aa3b, v133
	v_mul_f32_e32 v134, 0x3fcc422a, v134
	v_mul_f32_e32 v120, 0xbfb8aa3b, v120
	v_mul_f32_e32 v131, 0xbfb8aa3b, v131
	v_mul_f32_e32 v132, 0xbfb8aa3b, v132
	v_exp_f32_e32 v133, v133
	v_mul_f32_e32 v134, 0xbfb8aa3b, v134
	v_exp_f32_e32 v120, v120
	v_exp_f32_e32 v131, v131
	v_exp_f32_e32 v132, v132
	v_exp_f32_e32 v139, v134
	v_add_f32_e32 v133, 1.0, v133
	v_add_f32_e32 v120, 1.0, v120
	v_add_f32_e32 v131, 1.0, v131
	v_add_f32_e32 v132, 1.0, v132
	v_rcp_f32_e32 v134, v133
	v_add_f32_e32 v133, 1.0, v135
	v_add_f32_e32 v135, 1.0, v139
	v_rcp_f32_e32 v120, v120
	v_rcp_f32_e32 v121, v121
	v_rcp_f32_e32 v132, v132
	v_rcp_f32_e32 v133, v133
	v_rcp_f32_e32 v135, v135
	v_rcp_f32_e32 v131, v131
	v_pk_mul_f32 v[124:125], v[124:125], v[120:121]
	v_pk_mul_f32 v[126:127], v[126:127], v[132:133]
	v_pk_mul_f32 v[122:123], v[122:123], v[134:135]
	v_pk_mul_f32 v[128:129], v[128:129], v[130:131]
; DI unsigned pk_bf16(float lo, float hi) { const f32x2 v = {lo, hi}; return __builtin_bit_cast(unsigned, __builtin_convertvector(v, bf16x2_t)); }
; DI float gelu_tanh(float x) { const float u = 1.5957691216057308f * (x + 0.044715f * x * x * x); return x * sigmoidf_(u); }
; DI float sigmoidf_(float x) { return __builtin_amdgcn_rcpf(1.0f + __expf(-x)); }
;     DI void operator()(const f32x4 (&acc)[2][2][4][2], const Unit& u, int wr, int wc, int fr, int fq) const {
;     ...
;             for (int m = 0; m < 4; ++m) { bf16_t* rowp = base + (size_t)(u.orow + ai * 128 + wr * 64 + m * 16 + fr) * 1024 + colo;
; #pragma unroll
;                 for (int bj = 0; bj < 2; ++bj) { f32x4 v0 = acc[ai][bj][m][0] + bv[bj][0], v1 = acc[ai][bj][m][1] + bv[bj][1];
;                     if (isy) {
; #pragma unroll
;                         for (int j = 0; j < 4; ++j) { v0[j] = gelu_tanh(v0[j]); v1[j] = gelu_tanh(v1[j]); } }
;                     u32x4 w; w.x = pk_bf16(v0[0], v0[1]); w.y = pk_bf16(v0[2], v0[3]); w.z = pk_bf16(v1[0], v1[1]); w.w = pk_bf16(v1[2], v1[3]);
;                     *(u32x4*)(rowp + bj * 128) = w; } }
.LBB0_511:
	v_add_u32_e32 v120, 16, v138
	v_ashrrev_i32_e32 v121, 31, v120
	v_lshlrev_b64 v[120:121], 11, v[120:121]
	v_lshl_add_u64 v[120:121], v[136:137], 0, v[120:121]
	v_cvt_pk_bf16_f32 v124, v124, v125
	v_cvt_pk_bf16_f32 v125, v126, v127
	v_cvt_pk_bf16_f32 v126, v128, v129
	v_cvt_pk_bf16_f32 v127, v122, v123
	v_pk_add_f32 v[118:119], v[118:119], v[38:39]
	v_pk_add_f32 v[116:117], v[116:117], v[36:37]
	v_pk_add_f32 v[114:115], v[114:115], v[34:35]
	s_and_b64 vcc, exec, s[4:5]
	v_pk_add_f32 v[112:113], v[112:113], v[32:33]
	s_cbranch_vccnz .Lw_pl2
	global_store_dwordx4 v[120:121], v[124:127], off nt
	s_branch .Lw_dn2
.Lw_pl2:
	global_store_dwordx4 v[120:121], v[124:127], off
.Lw_dn2:
	s_cbranch_vccnz .LBB0_513
	v_mul_f32_e32 v123, 0x3d372713, v112
	v_mul_f32_e32 v123, v112, v123
	v_mul_f32_e32 v124, 0x3d372713, v117
	v_fma_f32 v123, v112, v123, v112
	v_mul_f32_e32 v124, v117, v124
	v_mov_b32_e32 v125, v117
	v_mul_f32_e32 v123, 0x3fcc422a, v123
	v_fmac_f32_e32 v125, v125, v124
	v_mul_f32_e32 v123, 0xbfb8aa3b, v123
	v_mul_f32_e32 v124, 0x3fcc422a, v125
	v_exp_f32_e32 v123, v123
	v_mul_f32_e32 v124, 0xbfb8aa3b, v124
	v_exp_f32_e32 v125, v124
	v_mul_f32_e32 v128, 0x3d372713, v119
	v_add_f32_e32 v123, 1.0, v123
	v_mul_f32_e32 v128, v119, v128
	v_rcp_f32_e32 v124, v123
	v_add_f32_e32 v123, 1.0, v125
	v_mul_f32_e32 v125, 0x3d372713, v113
	v_fma_f32 v128, v119, v128, v119
	v_mul_f32_e32 v125, v113, v125
	v_mov_b32_e32 v126, v113
	v_mul_f32_e32 v128, 0x3fcc422a, v128
	v_fmac_f32_e32 v126, v126, v125
	v_mul_f32_e32 v127, 0x3d372713, v114
	v_mul_f32_e32 v128, 0xbfb8aa3b, v128
	v_mul_f32_e32 v122, 0x3d372713, v116
	v_mul_f32_e32 v125, 0x3fcc422a, v126
	v_mul_f32_e32 v126, 0x3d372713, v118
	v_mul_f32_e32 v127, v114, v127
	v_exp_f32_e32 v129, v128
	v_mul_f32_e32 v128, 0x3d372713, v115
	v_mul_f32_e32 v122, v116, v122
	v_mul_f32_e32 v126, v118, v126
	v_fma_f32 v127, v114, v127, v114
	v_mul_f32_e32 v128, v115, v128
	v_fma_f32 v122, v116, v122, v116
	v_fma_f32 v126, v118, v126, v118
	v_mul_f32_e32 v127, 0x3fcc422a, v127
	v_fma_f32 v128, v115, v128, v115
	v_mul_f32_e32 v122, 0x3fcc422a, v122
	v_mul_f32_e32 v126, 0x3fcc422a, v126
	v_mul_f32_e32 v127, 0xbfb8aa3b, v127
	v_mul_f32_e32 v128, 0x3fcc422a, v128
	v_mul_f32_e32 v122, 0xbfb8aa3b, v122
	v_mul_f32_e32 v125, 0xbfb8aa3b, v125
	v_mul_f32_e32 v126, 0xbfb8aa3b, v126
	v_exp_f32_e32 v127, v127
	v_mul_f32_e32 v128, 0xbfb8aa3b, v128
	v_exp_f32_e32 v122, v122
	v_exp_f32_e32 v125, v125
	v_exp_f32_e32 v126, v126
	v_exp_f32_e32 v130, v128
	v_add_f32_e32 v127, 1.0, v127
	v_add_f32_e32 v122, 1.0, v122
	v_add_f32_e32 v125, 1.0, v125
	v_add_f32_e32 v126, 1.0, v126
	v_rcp_f32_e32 v128, v127
	v_add_f32_e32 v127, 1.0, v129
	v_add_f32_e32 v129, 1.0, v130
	v_rcp_f32_e32 v122, v122
	v_rcp_f32_e32 v123, v123
	v_rcp_f32_e32 v126, v126
	v_rcp_f32_e32 v127, v127
	v_rcp_f32_e32 v129, v129
	v_rcp_f32_e32 v125, v125
	v_pk_mul_f32 v[116:117], v[116:117], v[122:123]
	v_pk_mul_f32 v[118:119], v[118:119], v[126:127]
	v_pk_mul_f32 v[114:115], v[114:115], v[128:129]
	v_pk_mul_f32 v[112:113], v[112:113], v[124:125]
.LBB0_513:
	v_cvt_pk_bf16_f32 v116, v116, v117
	v_cvt_pk_bf16_f32 v117, v118, v119
	v_cvt_pk_bf16_f32 v118, v112, v113
	v_cvt_pk_bf16_f32 v119, v114, v115
	v_pk_add_f32 v[110:111], v[110:111], v[54:55]
	v_pk_add_f32 v[108:109], v[108:109], v[52:53]
	v_pk_add_f32 v[106:107], v[106:107], v[50:51]
	s_and_b64 vcc, exec, s[4:5]
	v_pk_add_f32 v[112:113], v[104:105], v[48:49]
	s_cbranch_vccnz .Lw_pl3
	global_store_dwordx4 v[120:121], v[116:119], off offset:256 nt
	s_branch .Lw_dn3
.Lw_pl3:
	global_store_dwordx4 v[120:121], v[116:119], off offset:256
.Lw_dn3:
	s_cbranch_vccnz .LBB0_515
	v_mul_f32_e32 v105, 0x3d372713, v112
	v_mul_f32_e32 v105, v112, v105
	v_mul_f32_e32 v114, 0x3d372713, v109
	v_fma_f32 v105, v112, v105, v112
	v_mul_f32_e32 v114, v109, v114
	v_mov_b32_e32 v115, v109
	v_mul_f32_e32 v105, 0x3fcc422a, v105
	v_fmac_f32_e32 v115, v115, v114
	v_mul_f32_e32 v105, 0xbfb8aa3b, v105
	v_mul_f32_e32 v114, 0x3fcc422a, v115
	v_exp_f32_e32 v105, v105
	v_mul_f32_e32 v114, 0xbfb8aa3b, v114
	v_exp_f32_e32 v115, v114
	v_mul_f32_e32 v118, 0x3d372713, v111
	v_add_f32_e32 v105, 1.0, v105
	v_mul_f32_e32 v118, v111, v118
	v_rcp_f32_e32 v114, v105
	v_add_f32_e32 v105, 1.0, v115
	v_mul_f32_e32 v115, 0x3d372713, v113
	v_fma_f32 v118, v111, v118, v111
	v_mul_f32_e32 v115, v113, v115
	v_mov_b32_e32 v116, v113
	v_mul_f32_e32 v118, 0x3fcc422a, v118
	v_fmac_f32_e32 v116, v116, v115
	v_mul_f32_e32 v117, 0x3d372713, v106
	v_mul_f32_e32 v118, 0xbfb8aa3b, v118
	v_mul_f32_e32 v104, 0x3d372713, v108
	v_mul_f32_e32 v115, 0x3fcc422a, v116
	v_mul_f32_e32 v116, 0x3d372713, v110
	v_mul_f32_e32 v117, v106, v117
	v_exp_f32_e32 v119, v118
	v_mul_f32_e32 v118, 0x3d372713, v107
	v_mul_f32_e32 v104, v108, v104
	v_mul_f32_e32 v116, v110, v116
	v_fma_f32 v117, v106, v117, v106
	v_mul_f32_e32 v118, v107, v118
	v_fma_f32 v104, v108, v104, v108
	v_fma_f32 v116, v110, v116, v110
	v_mul_f32_e32 v117, 0x3fcc422a, v117
	v_fma_f32 v118, v107, v118, v107
	v_mul_f32_e32 v104, 0x3fcc422a, v104
	v_mul_f32_e32 v116, 0x3fcc422a, v116
	v_mul_f32_e32 v117, 0xbfb8aa3b, v117
	v_mul_f32_e32 v118, 0x3fcc422a, v118
	v_mul_f32_e32 v104, 0xbfb8aa3b, v104
	v_mul_f32_e32 v115, 0xbfb8aa3b, v115
	v_mul_f32_e32 v116, 0xbfb8aa3b, v116
	v_exp_f32_e32 v117, v117
	v_mul_f32_e32 v118, 0xbfb8aa3b, v118
	v_exp_f32_e32 v104, v104
	v_exp_f32_e32 v115, v115
	v_exp_f32_e32 v116, v116
	v_exp_f32_e32 v120, v118
	v_add_f32_e32 v117, 1.0, v117
	v_add_f32_e32 v104, 1.0, v104
	v_add_f32_e32 v115, 1.0, v115
	v_add_f32_e32 v116, 1.0, v116
	v_rcp_f32_e32 v118, v117
	v_add_f32_e32 v117, 1.0, v119
	v_add_f32_e32 v119, 1.0, v120
	v_rcp_f32_e32 v104, v104
	v_rcp_f32_e32 v105, v105
	v_rcp_f32_e32 v116, v116
	v_rcp_f32_e32 v117, v117
	v_rcp_f32_e32 v119, v119
	v_rcp_f32_e32 v115, v115
	v_pk_mul_f32 v[108:109], v[108:109], v[104:105]
	v_pk_mul_f32 v[110:111], v[110:111], v[116:117]
	v_pk_mul_f32 v[106:107], v[106:107], v[118:119]
	v_pk_mul_f32 v[112:113], v[112:113], v[114:115]
; DI unsigned pk_bf16(float lo, float hi) { const f32x2 v = {lo, hi}; return __builtin_bit_cast(unsigned, __builtin_convertvector(v, bf16x2_t)); }
; DI float gelu_tanh(float x) { const float u = 1.5957691216057308f * (x + 0.044715f * x * x * x); return x * sigmoidf_(u); }
; DI float sigmoidf_(float x) { return __builtin_amdgcn_rcpf(1.0f + __expf(-x)); }
;     DI void operator()(const f32x4 (&acc)[2][2][4][2], const Unit& u, int wr, int wc, int fr, int fq) const {
;     ...
;             for (int m = 0; m < 4; ++m) { bf16_t* rowp = base + (size_t)(u.orow + ai * 128 + wr * 64 + m * 16 + fr) * 1024 + colo;
; #pragma unroll
;                 for (int bj = 0; bj < 2; ++bj) { f32x4 v0 = acc[ai][bj][m][0] + bv[bj][0], v1 = acc[ai][bj][m][1] + bv[bj][1];
;                     if (isy) {
; #pragma unroll
;                         for (int j = 0; j < 4; ++j) { v0[j] = gelu_tanh(v0[j]); v1[j] = gelu_tanh(v1[j]); } }
;                     u32x4 w; w.x = pk_bf16(v0[0], v0[1]); w.y = pk_bf16(v0[2], v0[3]); w.z = pk_bf16(v1[0], v1[1]); w.w = pk_bf16(v1[2], v1[3]);
;                     *(u32x4*)(rowp + bj * 128) = w; } }
.LBB0_515:
	v_add_u32_e32 v104, 32, v138
	v_ashrrev_i32_e32 v105, 31, v104
	v_lshlrev_b64 v[104:105], 11, v[104:105]
	v_lshl_add_u64 v[104:105], v[136:137], 0, v[104:105]
	v_cvt_pk_bf16_f32 v108, v108, v109
	v_cvt_pk_bf16_f32 v109, v110, v111
	v_cvt_pk_bf16_f32 v110, v112, v113
	v_cvt_pk_bf16_f32 v111, v106, v107
	v_pk_add_f32 v[102:103], v[102:103], v[38:39]
	v_pk_add_f32 v[100:101], v[100:101], v[36:37]
	v_pk_add_f32 v[98:99], v[98:99], v[34:35]
	s_and_b64 vcc, exec, s[4:5]
	v_pk_add_f32 v[96:97], v[96:97], v[32:33]
	s_cbranch_vccnz .Lw_pl4
	global_store_dwordx4 v[104:105], v[108:111], off nt
	s_branch .Lw_dn4
.Lw_pl4:
	global_store_dwordx4 v[104:105], v[108:111], off
.Lw_dn4:
	s_cbranch_vccnz .LBB0_517
	v_mul_f32_e32 v107, 0x3d372713, v96
	v_mul_f32_e32 v107, v96, v107
	v_mul_f32_e32 v108, 0x3d372713, v101
	v_fma_f32 v107, v96, v107, v96
	v_mul_f32_e32 v108, v101, v108
	v_mov_b32_e32 v109, v101
	v_mul_f32_e32 v107, 0x3fcc422a, v107
	v_fmac_f32_e32 v109, v109, v108
	v_mul_f32_e32 v107, 0xbfb8aa3b, v107
	v_mul_f32_e32 v108, 0x3fcc422a, v109
	v_exp_f32_e32 v107, v107
	v_mul_f32_e32 v108, 0xbfb8aa3b, v108
	v_exp_f32_e32 v109, v108
	v_mul_f32_e32 v112, 0x3d372713, v103
	v_add_f32_e32 v107, 1.0, v107
	v_mul_f32_e32 v112, v103, v112
	v_rcp_f32_e32 v108, v107
	v_add_f32_e32 v107, 1.0, v109
	v_mul_f32_e32 v109, 0x3d372713, v97
	v_fma_f32 v112, v103, v112, v103
	v_mul_f32_e32 v109, v97, v109
	v_mov_b32_e32 v110, v97
	v_mul_f32_e32 v112, 0x3fcc422a, v112
	v_fmac_f32_e32 v110, v110, v109
	v_mul_f32_e32 v111, 0x3d372713, v98
	v_mul_f32_e32 v112, 0xbfb8aa3b, v112
	v_mul_f32_e32 v106, 0x3d372713, v100
	v_mul_f32_e32 v109, 0x3fcc422a, v110
	v_mul_f32_e32 v110, 0x3d372713, v102
	v_mul_f32_e32 v111, v98, v111
	v_exp_f32_e32 v113, v112
	v_mul_f32_e32 v112, 0x3d372713, v99
	v_mul_f32_e32 v106, v100, v106
	v_mul_f32_e32 v110, v102, v110
	v_fma_f32 v111, v98, v111, v98
	v_mul_f32_e32 v112, v99, v112
	v_fma_f32 v106, v100, v106, v100
	v_fma_f32 v110, v102, v110, v102
	v_mul_f32_e32 v111, 0x3fcc422a, v111
	v_fma_f32 v112, v99, v112, v99
	v_mul_f32_e32 v106, 0x3fcc422a, v106
	v_mul_f32_e32 v110, 0x3fcc422a, v110
	v_mul_f32_e32 v111, 0xbfb8aa3b, v111
	v_mul_f32_e32 v112, 0x3fcc422a, v112
	v_mul_f32_e32 v106, 0xbfb8aa3b, v106
	v_mul_f32_e32 v109, 0xbfb8aa3b, v109
	v_mul_f32_e32 v110, 0xbfb8aa3b, v110
	v_exp_f32_e32 v111, v111
	v_mul_f32_e32 v112, 0xbfb8aa3b, v112
	v_exp_f32_e32 v106, v106
	v_exp_f32_e32 v109, v109
	v_exp_f32_e32 v110, v110
	v_exp_f32_e32 v114, v112
	v_add_f32_e32 v111, 1.0, v111
	v_add_f32_e32 v106, 1.0, v106
	v_add_f32_e32 v109, 1.0, v109
	v_add_f32_e32 v110, 1.0, v110
	v_rcp_f32_e32 v112, v111
	v_add_f32_e32 v111, 1.0, v113
	v_add_f32_e32 v113, 1.0, v114
	v_rcp_f32_e32 v106, v106
	v_rcp_f32_e32 v107, v107
	v_rcp_f32_e32 v110, v110
	v_rcp_f32_e32 v111, v111
	v_rcp_f32_e32 v113, v113
	v_rcp_f32_e32 v109, v109
	v_pk_mul_f32 v[100:101], v[100:101], v[106:107]
	v_pk_mul_f32 v[102:103], v[102:103], v[110:111]
	v_pk_mul_f32 v[98:99], v[98:99], v[112:113]
	v_pk_mul_f32 v[96:97], v[96:97], v[108:109]
.LBB0_517:
	v_cvt_pk_bf16_f32 v100, v100, v101
	v_cvt_pk_bf16_f32 v101, v102, v103
	v_cvt_pk_bf16_f32 v102, v96, v97
	v_cvt_pk_bf16_f32 v103, v98, v99
	v_pk_add_f32 v[94:95], v[94:95], v[54:55]
	v_pk_add_f32 v[92:93], v[92:93], v[52:53]
	v_pk_add_f32 v[90:91], v[90:91], v[50:51]
	s_and_b64 vcc, exec, s[4:5]
	v_pk_add_f32 v[96:97], v[88:89], v[48:49]
	s_cbranch_vccnz .Lw_pl5
	global_store_dwordx4 v[104:105], v[100:103], off offset:256 nt
	s_branch .Lw_dn5
.Lw_pl5:
	global_store_dwordx4 v[104:105], v[100:103], off offset:256
.Lw_dn5:
	s_cbranch_vccnz .LBB0_519
	v_mul_f32_e32 v89, 0x3d372713, v96
	v_mul_f32_e32 v89, v96, v89
	v_mul_f32_e32 v98, 0x3d372713, v93
	v_fma_f32 v89, v96, v89, v96
	v_mul_f32_e32 v98, v93, v98
	v_mov_b32_e32 v99, v93
	v_mul_f32_e32 v89, 0x3fcc422a, v89
	v_fmac_f32_e32 v99, v99, v98
	v_mul_f32_e32 v89, 0xbfb8aa3b, v89
	v_mul_f32_e32 v98, 0x3fcc422a, v99
	v_exp_f32_e32 v89, v89
	v_mul_f32_e32 v98, 0xbfb8aa3b, v98
	v_exp_f32_e32 v99, v98
	v_mul_f32_e32 v102, 0x3d372713, v95
	v_add_f32_e32 v89, 1.0, v89
	v_mul_f32_e32 v102, v95, v102
	v_rcp_f32_e32 v98, v89
	v_add_f32_e32 v89, 1.0, v99
	v_mul_f32_e32 v99, 0x3d372713, v97
	v_fma_f32 v102, v95, v102, v95
	v_mul_f32_e32 v99, v97, v99
	v_mov_b32_e32 v100, v97
	v_mul_f32_e32 v102, 0x3fcc422a, v102
	v_fmac_f32_e32 v100, v100, v99
	v_mul_f32_e32 v101, 0x3d372713, v90
	v_mul_f32_e32 v102, 0xbfb8aa3b, v102
	v_mul_f32_e32 v88, 0x3d372713, v92
	v_mul_f32_e32 v99, 0x3fcc422a, v100
	v_mul_f32_e32 v100, 0x3d372713, v94
	v_mul_f32_e32 v101, v90, v101
	v_exp_f32_e32 v103, v102
	v_mul_f32_e32 v102, 0x3d372713, v91
	v_mul_f32_e32 v88, v92, v88
	v_mul_f32_e32 v100, v94, v100
	v_fma_f32 v101, v90, v101, v90
	v_mul_f32_e32 v102, v91, v102
	v_fma_f32 v88, v92, v88, v92
	v_fma_f32 v100, v94, v100, v94
	v_mul_f32_e32 v101, 0x3fcc422a, v101
	v_fma_f32 v102, v91, v102, v91
	v_mul_f32_e32 v88, 0x3fcc422a, v88
	v_mul_f32_e32 v100, 0x3fcc422a, v100
	v_mul_f32_e32 v101, 0xbfb8aa3b, v101
	v_mul_f32_e32 v102, 0x3fcc422a, v102
	v_mul_f32_e32 v88, 0xbfb8aa3b, v88
	v_mul_f32_e32 v99, 0xbfb8aa3b, v99
	v_mul_f32_e32 v100, 0xbfb8aa3b, v100
	v_exp_f32_e32 v101, v101
	v_mul_f32_e32 v102, 0xbfb8aa3b, v102
	v_exp_f32_e32 v88, v88
	v_exp_f32_e32 v99, v99
	v_exp_f32_e32 v100, v100
	v_exp_f32_e32 v104, v102
	v_add_f32_e32 v101, 1.0, v101
	v_add_f32_e32 v88, 1.0, v88
	v_add_f32_e32 v99, 1.0, v99
	v_add_f32_e32 v100, 1.0, v100
	v_rcp_f32_e32 v102, v101
	v_add_f32_e32 v101, 1.0, v103
	v_add_f32_e32 v103, 1.0, v104
	v_rcp_f32_e32 v88, v88
	v_rcp_f32_e32 v89, v89
	v_rcp_f32_e32 v100, v100
	v_rcp_f32_e32 v101, v101
	v_rcp_f32_e32 v103, v103
	v_rcp_f32_e32 v99, v99
	v_pk_mul_f32 v[92:93], v[92:93], v[88:89]
	v_pk_mul_f32 v[94:95], v[94:95], v[100:101]
	v_pk_mul_f32 v[90:91], v[90:91], v[102:103]
	v_pk_mul_f32 v[96:97], v[96:97], v[98:99]
; DI unsigned pk_bf16(float lo, float hi) { const f32x2 v = {lo, hi}; return __builtin_bit_cast(unsigned, __builtin_convertvector(v, bf16x2_t)); }
; DI float gelu_tanh(float x) { const float u = 1.5957691216057308f * (x + 0.044715f * x * x * x); return x * sigmoidf_(u); }
; DI float sigmoidf_(float x) { return __builtin_amdgcn_rcpf(1.0f + __expf(-x)); }
;     DI void operator()(const f32x4 (&acc)[2][2][4][2], const Unit& u, int wr, int wc, int fr, int fq) const {
;     ...
;             for (int m = 0; m < 4; ++m) { bf16_t* rowp = base + (size_t)(u.orow + ai * 128 + wr * 64 + m * 16 + fr) * 1024 + colo;
; #pragma unroll
;                 for (int bj = 0; bj < 2; ++bj) { f32x4 v0 = acc[ai][bj][m][0] + bv[bj][0], v1 = acc[ai][bj][m][1] + bv[bj][1];
;                     if (isy) {
; #pragma unroll
;                         for (int j = 0; j < 4; ++j) { v0[j] = gelu_tanh(v0[j]); v1[j] = gelu_tanh(v1[j]); } }
;                     u32x4 w; w.x = pk_bf16(v0[0], v0[1]); w.y = pk_bf16(v0[2], v0[3]); w.z = pk_bf16(v1[0], v1[1]); w.w = pk_bf16(v1[2], v1[3]);
;                     *(u32x4*)(rowp + bj * 128) = w; } }
.LBB0_519:
	v_add_u32_e32 v88, 48, v138
	v_ashrrev_i32_e32 v89, 31, v88
	v_lshlrev_b64 v[88:89], 11, v[88:89]
	v_lshl_add_u64 v[88:89], v[136:137], 0, v[88:89]
	v_cvt_pk_bf16_f32 v92, v92, v93
	v_cvt_pk_bf16_f32 v93, v94, v95
	v_cvt_pk_bf16_f32 v94, v96, v97
	v_cvt_pk_bf16_f32 v95, v90, v91
	v_pk_add_f32 v[86:87], v[86:87], v[38:39]
	v_pk_add_f32 v[84:85], v[84:85], v[36:37]
	v_pk_add_f32 v[82:83], v[82:83], v[34:35]
	s_and_b64 vcc, exec, s[4:5]
	v_pk_add_f32 v[80:81], v[80:81], v[32:33]
	s_cbranch_vccnz .Lw_pl6
	global_store_dwordx4 v[88:89], v[92:95], off nt
	s_branch .Lw_dn6
.Lw_pl6:
	global_store_dwordx4 v[88:89], v[92:95], off
.Lw_dn6:
	s_cbranch_vccnz .LBB0_521
	v_mul_f32_e32 v91, 0x3d372713, v80
	v_mul_f32_e32 v91, v80, v91
	v_mul_f32_e32 v92, 0x3d372713, v85
	v_fma_f32 v91, v80, v91, v80
	v_mul_f32_e32 v92, v85, v92
	v_mov_b32_e32 v93, v85
	v_mul_f32_e32 v91, 0x3fcc422a, v91
	v_fmac_f32_e32 v93, v93, v92
	v_mul_f32_e32 v91, 0xbfb8aa3b, v91
	v_mul_f32_e32 v92, 0x3fcc422a, v93
	v_exp_f32_e32 v91, v91
	v_mul_f32_e32 v92, 0xbfb8aa3b, v92
	v_exp_f32_e32 v93, v92
	v_mul_f32_e32 v96, 0x3d372713, v87
	v_add_f32_e32 v91, 1.0, v91
	v_mul_f32_e32 v96, v87, v96
	v_rcp_f32_e32 v92, v91
	v_add_f32_e32 v91, 1.0, v93
	v_mul_f32_e32 v93, 0x3d372713, v81
	v_fma_f32 v96, v87, v96, v87
	v_mul_f32_e32 v93, v81, v93
	v_mov_b32_e32 v94, v81
	v_mul_f32_e32 v96, 0x3fcc422a, v96
	v_fmac_f32_e32 v94, v94, v93
	v_mul_f32_e32 v95, 0x3d372713, v82
	v_mul_f32_e32 v96, 0xbfb8aa3b, v96
	v_mul_f32_e32 v90, 0x3d372713, v84
	v_mul_f32_e32 v93, 0x3fcc422a, v94
	v_mul_f32_e32 v94, 0x3d372713, v86
	v_mul_f32_e32 v95, v82, v95
	v_exp_f32_e32 v97, v96
	v_mul_f32_e32 v96, 0x3d372713, v83
	v_mul_f32_e32 v90, v84, v90
	v_mul_f32_e32 v94, v86, v94
	v_fma_f32 v95, v82, v95, v82
	v_mul_f32_e32 v96, v83, v96
	v_fma_f32 v90, v84, v90, v84
	v_fma_f32 v94, v86, v94, v86
	v_mul_f32_e32 v95, 0x3fcc422a, v95
	v_fma_f32 v96, v83, v96, v83
	v_mul_f32_e32 v90, 0x3fcc422a, v90
	v_mul_f32_e32 v94, 0x3fcc422a, v94
	v_mul_f32_e32 v95, 0xbfb8aa3b, v95
	v_mul_f32_e32 v96, 0x3fcc422a, v96
	v_mul_f32_e32 v90, 0xbfb8aa3b, v90
	v_mul_f32_e32 v93, 0xbfb8aa3b, v93
	v_mul_f32_e32 v94, 0xbfb8aa3b, v94
	v_exp_f32_e32 v95, v95
	v_mul_f32_e32 v96, 0xbfb8aa3b, v96
	v_exp_f32_e32 v90, v90
	v_exp_f32_e32 v93, v93
	v_exp_f32_e32 v94, v94
	v_exp_f32_e32 v98, v96
	v_add_f32_e32 v95, 1.0, v95
	v_add_f32_e32 v90, 1.0, v90
	v_add_f32_e32 v93, 1.0, v93
	v_add_f32_e32 v94, 1.0, v94
	v_rcp_f32_e32 v96, v95
	v_add_f32_e32 v95, 1.0, v97
	v_add_f32_e32 v97, 1.0, v98
	v_rcp_f32_e32 v90, v90
	v_rcp_f32_e32 v91, v91
	v_rcp_f32_e32 v94, v94
	v_rcp_f32_e32 v95, v95
	v_rcp_f32_e32 v97, v97
	v_rcp_f32_e32 v93, v93
	v_pk_mul_f32 v[84:85], v[84:85], v[90:91]
	v_pk_mul_f32 v[86:87], v[86:87], v[94:95]
	v_pk_mul_f32 v[82:83], v[82:83], v[96:97]
	v_pk_mul_f32 v[80:81], v[80:81], v[92:93]
.LBB0_521:
	v_cvt_pk_bf16_f32 v84, v84, v85
	v_cvt_pk_bf16_f32 v85, v86, v87
	v_cvt_pk_bf16_f32 v86, v80, v81
	v_cvt_pk_bf16_f32 v87, v82, v83
	v_pk_add_f32 v[78:79], v[78:79], v[54:55]
	v_pk_add_f32 v[76:77], v[76:77], v[52:53]
	v_pk_add_f32 v[74:75], v[74:75], v[50:51]
	s_and_b64 vcc, exec, s[4:5]
	v_pk_add_f32 v[80:81], v[72:73], v[48:49]
	s_cbranch_vccnz .Lw_pl7
	global_store_dwordx4 v[88:89], v[84:87], off offset:256 nt
	s_branch .Lw_dn7
.Lw_pl7:
	global_store_dwordx4 v[88:89], v[84:87], off offset:256
.Lw_dn7:
	s_cbranch_vccnz .LBB0_523
	v_mul_f32_e32 v73, 0x3d372713, v80
	v_mul_f32_e32 v73, v80, v73
	v_mul_f32_e32 v82, 0x3d372713, v77
	v_fma_f32 v73, v80, v73, v80
	v_mul_f32_e32 v82, v77, v82
	v_mov_b32_e32 v83, v77
	v_mul_f32_e32 v73, 0x3fcc422a, v73
	v_fmac_f32_e32 v83, v83, v82
	v_mul_f32_e32 v73, 0xbfb8aa3b, v73
	v_mul_f32_e32 v82, 0x3fcc422a, v83
	v_exp_f32_e32 v73, v73
	v_mul_f32_e32 v82, 0xbfb8aa3b, v82
	v_exp_f32_e32 v83, v82
	v_mul_f32_e32 v86, 0x3d372713, v79
	v_add_f32_e32 v73, 1.0, v73
	v_mul_f32_e32 v86, v79, v86
	v_rcp_f32_e32 v82, v73
	v_add_f32_e32 v73, 1.0, v83
	v_mul_f32_e32 v83, 0x3d372713, v81
	v_fma_f32 v86, v79, v86, v79
	v_mul_f32_e32 v83, v81, v83
	v_mov_b32_e32 v84, v81
	v_mul_f32_e32 v86, 0x3fcc422a, v86
	v_fmac_f32_e32 v84, v84, v83
	v_mul_f32_e32 v85, 0x3d372713, v74
	v_mul_f32_e32 v86, 0xbfb8aa3b, v86
	v_mul_f32_e32 v72, 0x3d372713, v76
	v_mul_f32_e32 v83, 0x3fcc422a, v84
	v_mul_f32_e32 v84, 0x3d372713, v78
	v_mul_f32_e32 v85, v74, v85
	v_exp_f32_e32 v87, v86
	v_mul_f32_e32 v86, 0x3d372713, v75
	v_mul_f32_e32 v72, v76, v72
	v_mul_f32_e32 v84, v78, v84
	v_fma_f32 v85, v74, v85, v74
	v_mul_f32_e32 v86, v75, v86
	v_fma_f32 v72, v76, v72, v76
	v_fma_f32 v84, v78, v84, v78
	v_mul_f32_e32 v85, 0x3fcc422a, v85
	v_fma_f32 v86, v75, v86, v75
	v_mul_f32_e32 v72, 0x3fcc422a, v72
	v_mul_f32_e32 v84, 0x3fcc422a, v84
	v_mul_f32_e32 v85, 0xbfb8aa3b, v85
	v_mul_f32_e32 v86, 0x3fcc422a, v86
	v_mul_f32_e32 v72, 0xbfb8aa3b, v72
	v_mul_f32_e32 v83, 0xbfb8aa3b, v83
	v_mul_f32_e32 v84, 0xbfb8aa3b, v84
	v_exp_f32_e32 v85, v85
	v_mul_f32_e32 v86, 0xbfb8aa3b, v86
	v_exp_f32_e32 v72, v72
	v_exp_f32_e32 v83, v83
	v_exp_f32_e32 v84, v84
	v_exp_f32_e32 v88, v86
	v_add_f32_e32 v85, 1.0, v85
	v_add_f32_e32 v72, 1.0, v72
	v_add_f32_e32 v83, 1.0, v83
	v_add_f32_e32 v84, 1.0, v84
	v_rcp_f32_e32 v86, v85
	v_add_f32_e32 v85, 1.0, v87
	v_add_f32_e32 v87, 1.0, v88
	v_rcp_f32_e32 v72, v72
	v_rcp_f32_e32 v73, v73
	v_rcp_f32_e32 v84, v84
	v_rcp_f32_e32 v85, v85
	v_rcp_f32_e32 v87, v87
	v_rcp_f32_e32 v83, v83
	v_pk_mul_f32 v[76:77], v[76:77], v[72:73]
	v_pk_mul_f32 v[78:79], v[78:79], v[84:85]
	v_pk_mul_f32 v[74:75], v[74:75], v[86:87]
	v_pk_mul_f32 v[80:81], v[80:81], v[82:83]
; DI unsigned pk_bf16(float lo, float hi) { const f32x2 v = {lo, hi}; return __builtin_bit_cast(unsigned, __builtin_convertvector(v, bf16x2_t)); }
; DI float gelu_tanh(float x) { const float u = 1.5957691216057308f * (x + 0.044715f * x * x * x); return x * sigmoidf_(u); }
; DI float sigmoidf_(float x) { return __builtin_amdgcn_rcpf(1.0f + __expf(-x)); }
;     DI void operator()(const f32x4 (&acc)[2][2][4][2], const Unit& u, int wr, int wc, int fr, int fq) const {
;     ...
;             for (int m = 0; m < 4; ++m) { bf16_t* rowp = base + (size_t)(u.orow + ai * 128 + wr * 64 + m * 16 + fr) * 1024 + colo;
; #pragma unroll
;                 for (int bj = 0; bj < 2; ++bj) { f32x4 v0 = acc[ai][bj][m][0] + bv[bj][0], v1 = acc[ai][bj][m][1] + bv[bj][1];
;                     if (isy) {
; #pragma unroll
;                         for (int j = 0; j < 4; ++j) { v0[j] = gelu_tanh(v0[j]); v1[j] = gelu_tanh(v1[j]); } }
;                     u32x4 w; w.x = pk_bf16(v0[0], v0[1]); w.y = pk_bf16(v0[2], v0[3]); w.z = pk_bf16(v1[0], v1[1]); w.w = pk_bf16(v1[2], v1[3]);
;                     *(u32x4*)(rowp + bj * 128) = w; } }
.LBB0_523:
	v_add_u32_e32 v72, 0x80, v138
	v_ashrrev_i32_e32 v73, 31, v72
	v_lshlrev_b64 v[72:73], 11, v[72:73]
	v_lshl_add_u64 v[72:73], v[136:137], 0, v[72:73]
	v_cvt_pk_bf16_f32 v76, v76, v77
	v_cvt_pk_bf16_f32 v77, v78, v79
	v_cvt_pk_bf16_f32 v78, v80, v81
	v_cvt_pk_bf16_f32 v79, v74, v75
	v_pk_add_f32 v[70:71], v[70:71], v[38:39]
	v_pk_add_f32 v[68:69], v[68:69], v[36:37]
	v_pk_add_f32 v[66:67], v[66:67], v[34:35]
	s_and_b64 vcc, exec, s[4:5]
	v_pk_add_f32 v[64:65], v[64:65], v[32:33]
	s_cbranch_vccnz .Lw_pl8
	global_store_dwordx4 v[72:73], v[76:79], off nt
	s_branch .Lw_dn8
.Lw_pl8:
	global_store_dwordx4 v[72:73], v[76:79], off
.Lw_dn8:
	s_cbranch_vccnz .LBB0_525
	v_mul_f32_e32 v75, 0x3d372713, v64
	v_mul_f32_e32 v75, v64, v75
	v_mul_f32_e32 v76, 0x3d372713, v69
	v_fma_f32 v75, v64, v75, v64
	v_mul_f32_e32 v76, v69, v76
	v_mov_b32_e32 v77, v69
	v_mul_f32_e32 v75, 0x3fcc422a, v75
	v_fmac_f32_e32 v77, v77, v76
	v_mul_f32_e32 v75, 0xbfb8aa3b, v75
	v_mul_f32_e32 v76, 0x3fcc422a, v77
	v_exp_f32_e32 v75, v75
	v_mul_f32_e32 v76, 0xbfb8aa3b, v76
	v_exp_f32_e32 v77, v76
	v_mul_f32_e32 v80, 0x3d372713, v71
	v_add_f32_e32 v75, 1.0, v75
	v_mul_f32_e32 v80, v71, v80
	v_rcp_f32_e32 v76, v75
	v_add_f32_e32 v75, 1.0, v77
	v_mul_f32_e32 v77, 0x3d372713, v65
	v_fma_f32 v80, v71, v80, v71
	v_mul_f32_e32 v77, v65, v77
	v_mov_b32_e32 v78, v65
	v_mul_f32_e32 v80, 0x3fcc422a, v80
	v_fmac_f32_e32 v78, v78, v77
	v_mul_f32_e32 v79, 0x3d372713, v66
	v_mul_f32_e32 v80, 0xbfb8aa3b, v80
	v_mul_f32_e32 v74, 0x3d372713, v68
	v_mul_f32_e32 v77, 0x3fcc422a, v78
	v_mul_f32_e32 v78, 0x3d372713, v70
	v_mul_f32_e32 v79, v66, v79
	v_exp_f32_e32 v81, v80
	v_mul_f32_e32 v80, 0x3d372713, v67
	v_mul_f32_e32 v74, v68, v74
	v_mul_f32_e32 v78, v70, v78
	v_fma_f32 v79, v66, v79, v66
	v_mul_f32_e32 v80, v67, v80
	v_fma_f32 v74, v68, v74, v68
	v_fma_f32 v78, v70, v78, v70
	v_mul_f32_e32 v79, 0x3fcc422a, v79
	v_fma_f32 v80, v67, v80, v67
	v_mul_f32_e32 v74, 0x3fcc422a, v74
	v_mul_f32_e32 v78, 0x3fcc422a, v78
	v_mul_f32_e32 v79, 0xbfb8aa3b, v79
	v_mul_f32_e32 v80, 0x3fcc422a, v80
	v_mul_f32_e32 v74, 0xbfb8aa3b, v74
	v_mul_f32_e32 v77, 0xbfb8aa3b, v77
	v_mul_f32_e32 v78, 0xbfb8aa3b, v78
	v_exp_f32_e32 v79, v79
	v_mul_f32_e32 v80, 0xbfb8aa3b, v80
	v_exp_f32_e32 v74, v74
	v_exp_f32_e32 v77, v77
	v_exp_f32_e32 v78, v78
	v_exp_f32_e32 v82, v80
	v_add_f32_e32 v79, 1.0, v79
	v_add_f32_e32 v74, 1.0, v74
	v_add_f32_e32 v77, 1.0, v77
	v_add_f32_e32 v78, 1.0, v78
	v_rcp_f32_e32 v80, v79
	v_add_f32_e32 v79, 1.0, v81
	v_add_f32_e32 v81, 1.0, v82
	v_rcp_f32_e32 v74, v74
	v_rcp_f32_e32 v75, v75
	v_rcp_f32_e32 v78, v78
	v_rcp_f32_e32 v79, v79
	v_rcp_f32_e32 v81, v81
	v_rcp_f32_e32 v77, v77
	v_pk_mul_f32 v[68:69], v[68:69], v[74:75]
	v_pk_mul_f32 v[70:71], v[70:71], v[78:79]
	v_pk_mul_f32 v[66:67], v[66:67], v[80:81]
	v_pk_mul_f32 v[64:65], v[64:65], v[76:77]
.LBB0_525:
	v_cvt_pk_bf16_f32 v68, v68, v69
	v_cvt_pk_bf16_f32 v69, v70, v71
	v_cvt_pk_bf16_f32 v70, v64, v65
	v_cvt_pk_bf16_f32 v71, v66, v67
	v_pk_add_f32 v[62:63], v[62:63], v[54:55]
	v_pk_add_f32 v[60:61], v[60:61], v[52:53]
	v_pk_add_f32 v[58:59], v[58:59], v[50:51]
	s_and_b64 vcc, exec, s[4:5]
	v_pk_add_f32 v[64:65], v[56:57], v[48:49]
	s_cbranch_vccnz .Lw_pl9
	global_store_dwordx4 v[72:73], v[68:71], off offset:256 nt
	s_branch .Lw_dn9
.Lw_pl9:
	global_store_dwordx4 v[72:73], v[68:71], off offset:256
.Lw_dn9:
	s_cbranch_vccnz .LBB0_527
	v_mul_f32_e32 v57, 0x3d372713, v64
	v_mul_f32_e32 v57, v64, v57
	v_mul_f32_e32 v66, 0x3d372713, v61
	v_fma_f32 v57, v64, v57, v64
	v_mul_f32_e32 v66, v61, v66
	v_mov_b32_e32 v67, v61
	v_mul_f32_e32 v57, 0x3fcc422a, v57
	v_fmac_f32_e32 v67, v67, v66
	v_mul_f32_e32 v57, 0xbfb8aa3b, v57
	v_mul_f32_e32 v66, 0x3fcc422a, v67
	v_exp_f32_e32 v57, v57
	v_mul_f32_e32 v66, 0xbfb8aa3b, v66
	v_exp_f32_e32 v67, v66
	v_mul_f32_e32 v70, 0x3d372713, v63
	v_add_f32_e32 v57, 1.0, v57
	v_mul_f32_e32 v70, v63, v70
	v_rcp_f32_e32 v66, v57
	v_add_f32_e32 v57, 1.0, v67
	v_mul_f32_e32 v67, 0x3d372713, v65
	v_fma_f32 v70, v63, v70, v63
	v_mul_f32_e32 v67, v65, v67
	v_mov_b32_e32 v68, v65
	v_mul_f32_e32 v70, 0x3fcc422a, v70
	v_fmac_f32_e32 v68, v68, v67
	v_mul_f32_e32 v69, 0x3d372713, v58
	v_mul_f32_e32 v70, 0xbfb8aa3b, v70
	v_mul_f32_e32 v56, 0x3d372713, v60
	v_mul_f32_e32 v67, 0x3fcc422a, v68
	v_mul_f32_e32 v68, 0x3d372713, v62
	v_mul_f32_e32 v69, v58, v69
	v_exp_f32_e32 v71, v70
	v_mul_f32_e32 v70, 0x3d372713, v59
	v_mul_f32_e32 v56, v60, v56
	v_mul_f32_e32 v68, v62, v68
	v_fma_f32 v69, v58, v69, v58
	v_mul_f32_e32 v70, v59, v70
	v_fma_f32 v56, v60, v56, v60
	v_fma_f32 v68, v62, v68, v62
	v_mul_f32_e32 v69, 0x3fcc422a, v69
	v_fma_f32 v70, v59, v70, v59
	v_mul_f32_e32 v56, 0x3fcc422a, v56
	v_mul_f32_e32 v68, 0x3fcc422a, v68
	v_mul_f32_e32 v69, 0xbfb8aa3b, v69
	v_mul_f32_e32 v70, 0x3fcc422a, v70
	v_mul_f32_e32 v56, 0xbfb8aa3b, v56
	v_mul_f32_e32 v67, 0xbfb8aa3b, v67
	v_mul_f32_e32 v68, 0xbfb8aa3b, v68
	v_exp_f32_e32 v69, v69
	v_mul_f32_e32 v70, 0xbfb8aa3b, v70
	v_exp_f32_e32 v56, v56
	v_exp_f32_e32 v67, v67
	v_exp_f32_e32 v68, v68
	v_exp_f32_e32 v72, v70
	v_add_f32_e32 v69, 1.0, v69
	v_add_f32_e32 v56, 1.0, v56
	v_add_f32_e32 v67, 1.0, v67
	v_add_f32_e32 v68, 1.0, v68
	v_rcp_f32_e32 v70, v69
	v_add_f32_e32 v69, 1.0, v71
	v_add_f32_e32 v71, 1.0, v72
	v_rcp_f32_e32 v56, v56
	v_rcp_f32_e32 v57, v57
	v_rcp_f32_e32 v68, v68
	v_rcp_f32_e32 v69, v69
	v_rcp_f32_e32 v71, v71
	v_rcp_f32_e32 v67, v67
	v_pk_mul_f32 v[60:61], v[60:61], v[56:57]
	v_pk_mul_f32 v[62:63], v[62:63], v[68:69]
	v_pk_mul_f32 v[58:59], v[58:59], v[70:71]
	v_pk_mul_f32 v[64:65], v[64:65], v[66:67]
; DI unsigned pk_bf16(float lo, float hi) { const f32x2 v = {lo, hi}; return __builtin_bit_cast(unsigned, __builtin_convertvector(v, bf16x2_t)); }
; DI float gelu_tanh(float x) { const float u = 1.5957691216057308f * (x + 0.044715f * x * x * x); return x * sigmoidf_(u); }
; DI float sigmoidf_(float x) { return __builtin_amdgcn_rcpf(1.0f + __expf(-x)); }
;     DI void operator()(const f32x4 (&acc)[2][2][4][2], const Unit& u, int wr, int wc, int fr, int fq) const {
;     ...
;             for (int m = 0; m < 4; ++m) { bf16_t* rowp = base + (size_t)(u.orow + ai * 128 + wr * 64 + m * 16 + fr) * 1024 + colo;
; #pragma unroll
;                 for (int bj = 0; bj < 2; ++bj) { f32x4 v0 = acc[ai][bj][m][0] + bv[bj][0], v1 = acc[ai][bj][m][1] + bv[bj][1];
;                     if (isy) {
; #pragma unroll
;                         for (int j = 0; j < 4; ++j) { v0[j] = gelu_tanh(v0[j]); v1[j] = gelu_tanh(v1[j]); } }
;                     u32x4 w; w.x = pk_bf16(v0[0], v0[1]); w.y = pk_bf16(v0[2], v0[3]); w.z = pk_bf16(v1[0], v1[1]); w.w = pk_bf16(v1[2], v1[3]);
;                     *(u32x4*)(rowp + bj * 128) = w; } }
.LBB0_527:
	v_add_u32_e32 v56, 0x90, v138
	v_ashrrev_i32_e32 v57, 31, v56
	v_lshlrev_b64 v[56:57], 11, v[56:57]
	v_lshl_add_u64 v[56:57], v[136:137], 0, v[56:57]
	v_cvt_pk_bf16_f32 v60, v60, v61
	v_cvt_pk_bf16_f32 v61, v62, v63
	v_cvt_pk_bf16_f32 v62, v64, v65
	v_cvt_pk_bf16_f32 v63, v58, v59
	v_pk_add_f32 v[46:47], v[46:47], v[38:39]
	v_pk_add_f32 v[44:45], v[44:45], v[36:37]
	v_pk_add_f32 v[42:43], v[42:43], v[34:35]
	s_and_b64 vcc, exec, s[4:5]
	v_pk_add_f32 v[40:41], v[40:41], v[32:33]
	s_cbranch_vccnz .Lw_pl10
	global_store_dwordx4 v[56:57], v[60:63], off nt
	s_branch .Lw_dn10
.Lw_pl10:
	global_store_dwordx4 v[56:57], v[60:63], off
.Lw_dn10:
	s_cbranch_vccnz .LBB0_529
	v_mul_f32_e32 v59, 0x3d372713, v40
	v_mul_f32_e32 v59, v40, v59
	v_mul_f32_e32 v60, 0x3d372713, v45
	v_fma_f32 v59, v40, v59, v40
	v_mul_f32_e32 v60, v45, v60
	v_mov_b32_e32 v61, v45
	v_mul_f32_e32 v59, 0x3fcc422a, v59
	v_fmac_f32_e32 v61, v61, v60
	v_mul_f32_e32 v59, 0xbfb8aa3b, v59
	v_mul_f32_e32 v60, 0x3fcc422a, v61
	v_exp_f32_e32 v59, v59
	v_mul_f32_e32 v60, 0xbfb8aa3b, v60
	v_exp_f32_e32 v61, v60
	v_mul_f32_e32 v64, 0x3d372713, v47
	v_add_f32_e32 v59, 1.0, v59
	v_mul_f32_e32 v64, v47, v64
	v_rcp_f32_e32 v60, v59
	v_add_f32_e32 v59, 1.0, v61
	v_mul_f32_e32 v61, 0x3d372713, v41
	v_fma_f32 v64, v47, v64, v47
	v_mul_f32_e32 v61, v41, v61
	v_mov_b32_e32 v62, v41
	v_mul_f32_e32 v64, 0x3fcc422a, v64
	v_fmac_f32_e32 v62, v62, v61
	v_mul_f32_e32 v63, 0x3d372713, v42
	v_mul_f32_e32 v64, 0xbfb8aa3b, v64
	v_mul_f32_e32 v58, 0x3d372713, v44
	v_mul_f32_e32 v61, 0x3fcc422a, v62
	v_mul_f32_e32 v62, 0x3d372713, v46
	v_mul_f32_e32 v63, v42, v63
	v_exp_f32_e32 v65, v64
	v_mul_f32_e32 v64, 0x3d372713, v43
	v_mul_f32_e32 v58, v44, v58
	v_mul_f32_e32 v62, v46, v62
	v_fma_f32 v63, v42, v63, v42
	v_mul_f32_e32 v64, v43, v64
	v_fma_f32 v58, v44, v58, v44
	v_fma_f32 v62, v46, v62, v46
	v_mul_f32_e32 v63, 0x3fcc422a, v63
	v_fma_f32 v64, v43, v64, v43
	v_mul_f32_e32 v58, 0x3fcc422a, v58
	v_mul_f32_e32 v62, 0x3fcc422a, v62
	v_mul_f32_e32 v63, 0xbfb8aa3b, v63
	v_mul_f32_e32 v64, 0x3fcc422a, v64
	v_mul_f32_e32 v58, 0xbfb8aa3b, v58
	v_mul_f32_e32 v61, 0xbfb8aa3b, v61
	v_mul_f32_e32 v62, 0xbfb8aa3b, v62
	v_exp_f32_e32 v63, v63
	v_mul_f32_e32 v64, 0xbfb8aa3b, v64
	v_exp_f32_e32 v58, v58
	v_exp_f32_e32 v61, v61
	v_exp_f32_e32 v62, v62
	v_exp_f32_e32 v66, v64
	v_add_f32_e32 v63, 1.0, v63
	v_add_f32_e32 v58, 1.0, v58
	v_add_f32_e32 v61, 1.0, v61
	v_add_f32_e32 v62, 1.0, v62
	v_rcp_f32_e32 v64, v63
	v_add_f32_e32 v63, 1.0, v65
	v_add_f32_e32 v65, 1.0, v66
	v_rcp_f32_e32 v58, v58
	v_rcp_f32_e32 v59, v59
	v_rcp_f32_e32 v62, v62
	v_rcp_f32_e32 v63, v63
	v_rcp_f32_e32 v65, v65
	v_rcp_f32_e32 v61, v61
	v_pk_mul_f32 v[44:45], v[44:45], v[58:59]
	v_pk_mul_f32 v[46:47], v[46:47], v[62:63]
	v_pk_mul_f32 v[42:43], v[42:43], v[64:65]
	v_pk_mul_f32 v[40:41], v[40:41], v[60:61]
.LBB0_529:
	v_cvt_pk_bf16_f32 v44, v44, v45
	v_cvt_pk_bf16_f32 v45, v46, v47
	v_cvt_pk_bf16_f32 v46, v40, v41
	v_cvt_pk_bf16_f32 v47, v42, v43
	v_pk_add_f32 v[30:31], v[30:31], v[54:55]
	v_pk_add_f32 v[28:29], v[28:29], v[52:53]
	v_pk_add_f32 v[26:27], v[26:27], v[50:51]
	s_and_b64 vcc, exec, s[4:5]
	v_pk_add_f32 v[40:41], v[24:25], v[48:49]
	s_cbranch_vccnz .Lw_pl11
	global_store_dwordx4 v[56:57], v[44:47], off offset:256 nt
	s_branch .Lw_dn11
.Lw_pl11:
	global_store_dwordx4 v[56:57], v[44:47], off offset:256
.Lw_dn11:
	s_cbranch_vccnz .LBB0_531
	v_mul_f32_e32 v25, 0x3d372713, v40
	v_mul_f32_e32 v25, v40, v25
	v_mul_f32_e32 v42, 0x3d372713, v29
	v_fma_f32 v25, v40, v25, v40
	v_mul_f32_e32 v42, v29, v42
	v_mov_b32_e32 v43, v29
	v_mul_f32_e32 v25, 0x3fcc422a, v25
	v_fmac_f32_e32 v43, v43, v42
	v_mul_f32_e32 v25, 0xbfb8aa3b, v25
	v_mul_f32_e32 v42, 0x3fcc422a, v43
	v_exp_f32_e32 v25, v25
	v_mul_f32_e32 v42, 0xbfb8aa3b, v42
	v_exp_f32_e32 v43, v42
	v_mul_f32_e32 v46, 0x3d372713, v31
	v_add_f32_e32 v25, 1.0, v25
	v_mul_f32_e32 v46, v31, v46
	v_rcp_f32_e32 v42, v25
	v_add_f32_e32 v25, 1.0, v43
	v_mul_f32_e32 v43, 0x3d372713, v41
	v_fma_f32 v46, v31, v46, v31
	v_mul_f32_e32 v43, v41, v43
	v_mov_b32_e32 v44, v41
	v_mul_f32_e32 v46, 0x3fcc422a, v46
	v_fmac_f32_e32 v44, v44, v43
	v_mul_f32_e32 v45, 0x3d372713, v26
	v_mul_f32_e32 v46, 0xbfb8aa3b, v46
	v_mul_f32_e32 v24, 0x3d372713, v28
	v_mul_f32_e32 v43, 0x3fcc422a, v44
	v_mul_f32_e32 v44, 0x3d372713, v30
	v_mul_f32_e32 v45, v26, v45
	v_exp_f32_e32 v47, v46
	v_mul_f32_e32 v46, 0x3d372713, v27
	v_mul_f32_e32 v24, v28, v24
	v_mul_f32_e32 v44, v30, v44
	v_fma_f32 v45, v26, v45, v26
	v_mul_f32_e32 v46, v27, v46
	v_fma_f32 v24, v28, v24, v28
	v_fma_f32 v44, v30, v44, v30
	v_mul_f32_e32 v45, 0x3fcc422a, v45
	v_fma_f32 v46, v27, v46, v27
	v_mul_f32_e32 v24, 0x3fcc422a, v24
	v_mul_f32_e32 v44, 0x3fcc422a, v44
	v_mul_f32_e32 v45, 0xbfb8aa3b, v45
	v_mul_f32_e32 v46, 0x3fcc422a, v46
	v_mul_f32_e32 v24, 0xbfb8aa3b, v24
	v_mul_f32_e32 v43, 0xbfb8aa3b, v43
	v_mul_f32_e32 v44, 0xbfb8aa3b, v44
	v_exp_f32_e32 v45, v45
	v_mul_f32_e32 v46, 0xbfb8aa3b, v46
	v_exp_f32_e32 v24, v24
	v_exp_f32_e32 v43, v43
	v_exp_f32_e32 v44, v44
	v_exp_f32_e32 v56, v46
	v_add_f32_e32 v45, 1.0, v45
	v_add_f32_e32 v24, 1.0, v24
	v_add_f32_e32 v43, 1.0, v43
	v_add_f32_e32 v44, 1.0, v44
	v_rcp_f32_e32 v46, v45
	v_add_f32_e32 v45, 1.0, v47
	v_add_f32_e32 v47, 1.0, v56
	v_rcp_f32_e32 v24, v24
	v_rcp_f32_e32 v25, v25
	v_rcp_f32_e32 v44, v44
	v_rcp_f32_e32 v45, v45
	v_rcp_f32_e32 v47, v47
	v_rcp_f32_e32 v43, v43
	v_pk_mul_f32 v[28:29], v[28:29], v[24:25]
	v_pk_mul_f32 v[30:31], v[30:31], v[44:45]
	v_pk_mul_f32 v[26:27], v[26:27], v[46:47]
	v_pk_mul_f32 v[40:41], v[40:41], v[42:43]
; DI unsigned pk_bf16(float lo, float hi) { const f32x2 v = {lo, hi}; return __builtin_bit_cast(unsigned, __builtin_convertvector(v, bf16x2_t)); }
; DI float gelu_tanh(float x) { const float u = 1.5957691216057308f * (x + 0.044715f * x * x * x); return x * sigmoidf_(u); }
; DI float sigmoidf_(float x) { return __builtin_amdgcn_rcpf(1.0f + __expf(-x)); }
;     DI void operator()(const f32x4 (&acc)[2][2][4][2], const Unit& u, int wr, int wc, int fr, int fq) const {
;     ...
;             for (int m = 0; m < 4; ++m) { bf16_t* rowp = base + (size_t)(u.orow + ai * 128 + wr * 64 + m * 16 + fr) * 1024 + colo;
; #pragma unroll
;                 for (int bj = 0; bj < 2; ++bj) { f32x4 v0 = acc[ai][bj][m][0] + bv[bj][0], v1 = acc[ai][bj][m][1] + bv[bj][1];
;                     if (isy) {
; #pragma unroll
;                         for (int j = 0; j < 4; ++j) { v0[j] = gelu_tanh(v0[j]); v1[j] = gelu_tanh(v1[j]); } }
;                     u32x4 w; w.x = pk_bf16(v0[0], v0[1]); w.y = pk_bf16(v0[2], v0[3]); w.z = pk_bf16(v1[0], v1[1]); w.w = pk_bf16(v1[2], v1[3]);
;                     *(u32x4*)(rowp + bj * 128) = w; } }
.LBB0_531:
	v_add_u32_e32 v24, 0xa0, v138
	v_ashrrev_i32_e32 v25, 31, v24
	v_lshlrev_b64 v[24:25], 11, v[24:25]
	v_lshl_add_u64 v[24:25], v[136:137], 0, v[24:25]
	v_cvt_pk_bf16_f32 v28, v28, v29
	v_cvt_pk_bf16_f32 v29, v30, v31
	v_cvt_pk_bf16_f32 v30, v40, v41
	v_cvt_pk_bf16_f32 v31, v26, v27
	v_pk_add_f32 v[22:23], v[22:23], v[38:39]
	v_pk_add_f32 v[20:21], v[20:21], v[36:37]
	v_pk_add_f32 v[18:19], v[18:19], v[34:35]
	s_and_b64 vcc, exec, s[4:5]
	v_pk_add_f32 v[16:17], v[16:17], v[32:33]
	s_cbranch_vccnz .Lw_pl12
	global_store_dwordx4 v[24:25], v[28:31], off nt
	s_branch .Lw_dn12
.Lw_pl12:
	global_store_dwordx4 v[24:25], v[28:31], off
.Lw_dn12:
	s_cbranch_vccnz .LBB0_533
	v_mul_f32_e32 v27, 0x3d372713, v16
	v_mul_f32_e32 v27, v16, v27
	v_mul_f32_e32 v28, 0x3d372713, v21
	v_fma_f32 v27, v16, v27, v16
	v_mul_f32_e32 v28, v21, v28
	v_mov_b32_e32 v29, v21
	v_mul_f32_e32 v27, 0x3fcc422a, v27
	v_fmac_f32_e32 v29, v29, v28
	v_mul_f32_e32 v27, 0xbfb8aa3b, v27
	v_mul_f32_e32 v28, 0x3fcc422a, v29
	v_exp_f32_e32 v27, v27
	v_mul_f32_e32 v28, 0xbfb8aa3b, v28
	v_exp_f32_e32 v29, v28
	v_mul_f32_e32 v40, 0x3d372713, v23
	v_add_f32_e32 v27, 1.0, v27
	v_mul_f32_e32 v40, v23, v40
	v_rcp_f32_e32 v28, v27
	v_add_f32_e32 v27, 1.0, v29
	v_mul_f32_e32 v29, 0x3d372713, v17
	v_fma_f32 v40, v23, v40, v23
	v_mul_f32_e32 v29, v17, v29
	v_mov_b32_e32 v30, v17
	v_mul_f32_e32 v40, 0x3fcc422a, v40
	v_fmac_f32_e32 v30, v30, v29
	v_mul_f32_e32 v31, 0x3d372713, v18
	v_mul_f32_e32 v40, 0xbfb8aa3b, v40
	v_mul_f32_e32 v26, 0x3d372713, v20
	v_mul_f32_e32 v29, 0x3fcc422a, v30
	v_mul_f32_e32 v30, 0x3d372713, v22
	v_mul_f32_e32 v31, v18, v31
	v_exp_f32_e32 v41, v40
	v_mul_f32_e32 v40, 0x3d372713, v19
	v_mul_f32_e32 v26, v20, v26
	v_mul_f32_e32 v30, v22, v30
	v_fma_f32 v31, v18, v31, v18
	v_mul_f32_e32 v40, v19, v40
	v_fma_f32 v26, v20, v26, v20
	v_fma_f32 v30, v22, v30, v22
	v_mul_f32_e32 v31, 0x3fcc422a, v31
	v_fma_f32 v40, v19, v40, v19
	v_mul_f32_e32 v26, 0x3fcc422a, v26
	v_mul_f32_e32 v30, 0x3fcc422a, v30
	v_mul_f32_e32 v31, 0xbfb8aa3b, v31
	v_mul_f32_e32 v40, 0x3fcc422a, v40
	v_mul_f32_e32 v26, 0xbfb8aa3b, v26
	v_mul_f32_e32 v29, 0xbfb8aa3b, v29
	v_mul_f32_e32 v30, 0xbfb8aa3b, v30
	v_exp_f32_e32 v31, v31
	v_mul_f32_e32 v40, 0xbfb8aa3b, v40
	v_exp_f32_e32 v26, v26
	v_exp_f32_e32 v29, v29
	v_exp_f32_e32 v30, v30
	v_exp_f32_e32 v42, v40
	v_add_f32_e32 v31, 1.0, v31
	v_add_f32_e32 v26, 1.0, v26
	v_add_f32_e32 v29, 1.0, v29
	v_add_f32_e32 v30, 1.0, v30
	v_rcp_f32_e32 v40, v31
	v_add_f32_e32 v31, 1.0, v41
	v_add_f32_e32 v41, 1.0, v42
	v_rcp_f32_e32 v26, v26
	v_rcp_f32_e32 v27, v27
	v_rcp_f32_e32 v30, v30
	v_rcp_f32_e32 v31, v31
	v_rcp_f32_e32 v41, v41
	v_rcp_f32_e32 v29, v29
	v_pk_mul_f32 v[20:21], v[20:21], v[26:27]
	v_pk_mul_f32 v[22:23], v[22:23], v[30:31]
	v_pk_mul_f32 v[18:19], v[18:19], v[40:41]
	v_pk_mul_f32 v[16:17], v[16:17], v[28:29]
.LBB0_533:
	v_cvt_pk_bf16_f32 v20, v20, v21
	v_cvt_pk_bf16_f32 v21, v22, v23
	v_cvt_pk_bf16_f32 v22, v16, v17
	v_cvt_pk_bf16_f32 v23, v18, v19
	v_pk_add_f32 v[14:15], v[14:15], v[54:55]
	v_pk_add_f32 v[12:13], v[12:13], v[52:53]
	v_pk_add_f32 v[10:11], v[10:11], v[50:51]
	s_and_b64 vcc, exec, s[4:5]
	v_pk_add_f32 v[16:17], v[8:9], v[48:49]
	s_cbranch_vccnz .Lw_pl13
	global_store_dwordx4 v[24:25], v[20:23], off offset:256 nt
	s_branch .Lw_dn13
.Lw_pl13:
	global_store_dwordx4 v[24:25], v[20:23], off offset:256
; DI unsigned pk_bf16(float lo, float hi) { const f32x2 v = {lo, hi}; return __builtin_bit_cast(unsigned, __builtin_convertvector(v, bf16x2_t)); }
; DI float gelu_tanh(float x) { const float u = 1.5957691216057308f * (x + 0.044715f * x * x * x); return x * sigmoidf_(u); }
; #define PG8_BAR __builtin_amdgcn_s_barrier()
; template <class Epi, class Sched>
; DI void gemm_phase(LAS unsigned char* lds, const int tid, const int K, const unsigned lda_bytes, const Sched& S, const Epi& E) {
;     ...
;         cur = nxt; cA = nA; cB = nB; ++ui;
; #pragma unroll
;         for (int i = 0; i < 2; ++i) { vA0[i] = o0[i]; vA1[i] = o1[i]; }
;         if (wr == 1) PG8_BAR;
;     DI void operator()(const f32x4 (&acc)[2][2][4][2], const Unit& u, int wr, int wc, int fr, int fq) const {
;     ...
;             for (int m = 0; m < 4; ++m) { bf16_t* rowp = base + (size_t)(u.orow + ai * 128 + wr * 64 + m * 16 + fr) * 1024 + colo;
; #pragma unroll
;                 for (int bj = 0; bj < 2; ++bj) { f32x4 v0 = acc[ai][bj][m][0] + bv[bj][0], v1 = acc[ai][bj][m][1] + bv[bj][1];
;                     if (isy) {
; #pragma unroll
;                         for (int j = 0; j < 4; ++j) { v0[j] = gelu_tanh(v0[j]); v1[j] = gelu_tanh(v1[j]); } }
;                     u32x4 w; w.x = pk_bf16(v0[0], v0[1]); w.y = pk_bf16(v0[2], v0[3]); w.z = pk_bf16(v1[0], v1[1]); w.w = pk_bf16(v1[2], v1[3]);
;                     *(u32x4*)(rowp + bj * 128) = w; } }
.Lw_dn13:
	s_cbranch_vccnz .LBB0_535
	v_mul_f32_e32 v9, 0x3d372713, v16
	v_mul_f32_e32 v9, v16, v9
	v_mul_f32_e32 v18, 0x3d372713, v13
	v_fma_f32 v9, v16, v9, v16
	v_mul_f32_e32 v18, v13, v18
	v_mov_b32_e32 v19, v13
	v_mul_f32_e32 v9, 0x3fcc422a, v9
	v_fmac_f32_e32 v19, v19, v18
	v_mul_f32_e32 v9, 0xbfb8aa3b, v9
	v_mul_f32_e32 v18, 0x3fcc422a, v19
	v_exp_f32_e32 v9, v9
	v_mul_f32_e32 v18, 0xbfb8aa3b, v18
	v_exp_f32_e32 v19, v18
	v_mul_f32_e32 v22, 0x3d372713, v15
	v_add_f32_e32 v9, 1.0, v9
	v_mul_f32_e32 v22, v15, v22
	v_rcp_f32_e32 v18, v9
	v_add_f32_e32 v9, 1.0, v19
	v_mul_f32_e32 v19, 0x3d372713, v17
	v_fma_f32 v22, v15, v22, v15
	v_mul_f32_e32 v19, v17, v19
	v_mov_b32_e32 v20, v17
	v_mul_f32_e32 v22, 0x3fcc422a, v22
	v_fmac_f32_e32 v20, v20, v19
	v_mul_f32_e32 v21, 0x3d372713, v10
	v_mul_f32_e32 v22, 0xbfb8aa3b, v22
	v_mul_f32_e32 v8, 0x3d372713, v12
	v_mul_f32_e32 v19, 0x3fcc422a, v20
	v_mul_f32_e32 v20, 0x3d372713, v14
	v_mul_f32_e32 v21, v10, v21
	v_exp_f32_e32 v23, v22
	v_mul_f32_e32 v22, 0x3d372713, v11
	v_mul_f32_e32 v8, v12, v8
	v_mul_f32_e32 v20, v14, v20
	v_fma_f32 v21, v10, v21, v10
	v_mul_f32_e32 v22, v11, v22
	v_fma_f32 v8, v12, v8, v12
	v_fma_f32 v20, v14, v20, v14
	v_mul_f32_e32 v21, 0x3fcc422a, v21
	v_fma_f32 v22, v11, v22, v11
	v_mul_f32_e32 v8, 0x3fcc422a, v8
	v_mul_f32_e32 v20, 0x3fcc422a, v20
	v_mul_f32_e32 v21, 0xbfb8aa3b, v21
	v_mul_f32_e32 v22, 0x3fcc422a, v22
	v_mul_f32_e32 v8, 0xbfb8aa3b, v8
	v_mul_f32_e32 v19, 0xbfb8aa3b, v19
	v_mul_f32_e32 v20, 0xbfb8aa3b, v20
	v_exp_f32_e32 v21, v21
	v_mul_f32_e32 v22, 0xbfb8aa3b, v22
	v_exp_f32_e32 v8, v8
	v_exp_f32_e32 v19, v19
	v_exp_f32_e32 v20, v20
	v_exp_f32_e32 v24, v22
	v_add_f32_e32 v21, 1.0, v21
	v_add_f32_e32 v8, 1.0, v8
	v_add_f32_e32 v19, 1.0, v19
	v_add_f32_e32 v20, 1.0, v20
	v_rcp_f32_e32 v22, v21
	v_add_f32_e32 v21, 1.0, v23
	v_add_f32_e32 v23, 1.0, v24
	v_rcp_f32_e32 v8, v8
	v_rcp_f32_e32 v9, v9
	v_rcp_f32_e32 v20, v20
	v_rcp_f32_e32 v21, v21
	v_rcp_f32_e32 v23, v23
	v_rcp_f32_e32 v19, v19
	v_pk_mul_f32 v[12:13], v[12:13], v[8:9]
	v_pk_mul_f32 v[14:15], v[14:15], v[20:21]
	v_pk_mul_f32 v[10:11], v[10:11], v[22:23]
	v_pk_mul_f32 v[16:17], v[16:17], v[18:19]
.LBB0_535:
	v_add_u32_e32 v8, 0xb0, v138
	v_ashrrev_i32_e32 v9, 31, v8
	v_lshlrev_b64 v[8:9], 11, v[8:9]
	v_lshl_add_u64 v[8:9], v[136:137], 0, v[8:9]
	v_cvt_pk_bf16_f32 v12, v12, v13
	v_cvt_pk_bf16_f32 v13, v14, v15
	v_cvt_pk_bf16_f32 v14, v16, v17
	v_cvt_pk_bf16_f32 v15, v10, v11
	v_pk_add_f32 v[6:7], v[6:7], v[38:39]
	v_pk_add_f32 v[4:5], v[4:5], v[36:37]
	v_pk_add_f32 v[2:3], v[2:3], v[34:35]
	s_and_b64 vcc, exec, s[4:5]
	v_pk_add_f32 v[0:1], v[0:1], v[32:33]
	s_cbranch_vccnz .Lw_pl14
	global_store_dwordx4 v[8:9], v[12:15], off nt
	s_branch .Lw_dn14
.Lw_pl14:
	global_store_dwordx4 v[8:9], v[12:15], off
.Lw_dn14:
	s_cbranch_vccnz .LBB0_537
	v_mul_f32_e32 v11, 0x3d372713, v0
	v_mul_f32_e32 v11, v0, v11
	v_mul_f32_e32 v12, 0x3d372713, v5
	v_fma_f32 v11, v0, v11, v0
	v_mul_f32_e32 v12, v5, v12
	v_mov_b32_e32 v13, v5
	v_mul_f32_e32 v11, 0x3fcc422a, v11
	v_fmac_f32_e32 v13, v13, v12
	v_mul_f32_e32 v11, 0xbfb8aa3b, v11
	v_mul_f32_e32 v12, 0x3fcc422a, v13
	v_exp_f32_e32 v11, v11
	v_mul_f32_e32 v12, 0xbfb8aa3b, v12
	v_exp_f32_e32 v13, v12
	v_mul_f32_e32 v16, 0x3d372713, v7
	v_add_f32_e32 v11, 1.0, v11
	v_mul_f32_e32 v16, v7, v16
	v_rcp_f32_e32 v12, v11
	v_add_f32_e32 v11, 1.0, v13
	v_mul_f32_e32 v13, 0x3d372713, v1
	v_fma_f32 v16, v7, v16, v7
	v_mul_f32_e32 v13, v1, v13
	v_mov_b32_e32 v14, v1
	v_mul_f32_e32 v16, 0x3fcc422a, v16
	v_fmac_f32_e32 v14, v14, v13
	v_mul_f32_e32 v15, 0x3d372713, v2
	v_mul_f32_e32 v16, 0xbfb8aa3b, v16
	v_mul_f32_e32 v10, 0x3d372713, v4
	v_mul_f32_e32 v13, 0x3fcc422a, v14
	v_mul_f32_e32 v14, 0x3d372713, v6
	v_mul_f32_e32 v15, v2, v15
	v_exp_f32_e32 v17, v16
	v_mul_f32_e32 v16, 0x3d372713, v3
	v_mul_f32_e32 v10, v4, v10
	v_mul_f32_e32 v14, v6, v14
	v_fma_f32 v15, v2, v15, v2
	v_mul_f32_e32 v16, v3, v16
	v_fma_f32 v10, v4, v10, v4
	v_fma_f32 v14, v6, v14, v6
	v_mul_f32_e32 v15, 0x3fcc422a, v15
	v_fma_f32 v16, v3, v16, v3
	v_mul_f32_e32 v10, 0x3fcc422a, v10
	v_mul_f32_e32 v14, 0x3fcc422a, v14
	v_mul_f32_e32 v15, 0xbfb8aa3b, v15
	v_mul_f32_e32 v16, 0x3fcc422a, v16
	v_mul_f32_e32 v10, 0xbfb8aa3b, v10
	v_mul_f32_e32 v13, 0xbfb8aa3b, v13
	v_mul_f32_e32 v14, 0xbfb8aa3b, v14
	v_exp_f32_e32 v15, v15
	v_mul_f32_e32 v16, 0xbfb8aa3b, v16
	v_exp_f32_e32 v10, v10
	v_exp_f32_e32 v13, v13
	v_exp_f32_e32 v14, v14
	v_exp_f32_e32 v18, v16
	v_add_f32_e32 v15, 1.0, v15
	v_add_f32_e32 v10, 1.0, v10
	v_add_f32_e32 v13, 1.0, v13
	v_add_f32_e32 v14, 1.0, v14
	v_rcp_f32_e32 v16, v15
	v_add_f32_e32 v15, 1.0, v17
	v_add_f32_e32 v17, 1.0, v18
	v_rcp_f32_e32 v10, v10
	v_rcp_f32_e32 v11, v11
	v_rcp_f32_e32 v14, v14
	v_rcp_f32_e32 v15, v15
	v_rcp_f32_e32 v17, v17
	v_rcp_f32_e32 v13, v13
	v_pk_mul_f32 v[4:5], v[4:5], v[10:11]
	v_pk_mul_f32 v[6:7], v[6:7], v[14:15]
	v_pk_mul_f32 v[2:3], v[2:3], v[16:17]
	v_pk_mul_f32 v[0:1], v[0:1], v[12:13]
.LBB0_537:
	v_cvt_pk_bf16_f32 v4, v4, v5
	v_cvt_pk_bf16_f32 v5, v6, v7
	v_cvt_pk_bf16_f32 v6, v0, v1
	v_cvt_pk_bf16_f32 v7, v2, v3
	s_andn2_b64 vcc, exec, s[2:3]
	s_mov_b64 s[0:1], -1
	s_cbranch_vccnz .Lw_pl15
	global_store_dwordx4 v[8:9], v[4:7], off offset:256 nt
	s_branch .Lw_dn15
.Lw_pl15:
	global_store_dwordx4 v[8:9], v[4:7], off offset:256
.Lw_dn15:
	s_cbranch_vccnz .LBB0_492
	s_andn2_b64 vcc, exec, s[14:15]
	s_cbranch_vccnz .LBB0_491
	s_barrier
	s_branch .LBB0_491

;     DI void operator()(const f32x4 (&acc)[2][2][4][2], const Unit& u, int wr, int wc, int fr, int fq) const {
;     ...
;             for (int m = 0; m < 4; ++m) { const size_t ro = (size_t)(u.orow + ai * 128 + wr * 64 + m * 16 + fr) * 1024 + col0;
; #pragma unroll
;                 for (int bj = 0; bj < 2; ++bj) {
;                     float h[8];
;                     if (x) { const f32x4 h0 = *(const f32x4*)(x + ro + bj * 128), h1 = *(const f32x4*)(x + ro + bj * 128 + 4); h[0] = h0[0]; h[1] = h0[1]; h[2] = h0[2]; h[3] = h0[3]; h[4] = h1[0]; h[5] = h1[1]; h[6] = h1[2]; h[7] = h1[3]; }
;                     else res8(*(const u32x4*)(HB + ro + bj * 128), *(const u32x4*)(HLO + ro + bj * 128), h);
.LBB0_884:
	v_add_u32_e32 v144, s58, v158
	v_lshl_or_b32 v142, s55, 8, v160
	v_ashrrev_i32_e32 v145, 31, v144
	v_ashrrev_i32_e32 v143, 31, v142
	v_lshlrev_b64 v[128:129], 10, v[144:145]
	v_lshl_add_u64 v[152:153], v[128:129], 0, v[142:143]
	v_cndmask_b32_e64 v128, 0, 1, s[24:25]
	v_cmp_ne_u32_e64 s[4:5], 1, v128
	s_andn2_b64 vcc, exec, s[24:25]
	v_lshl_add_u64 v[150:151], v[152:153], 2, s[18:19]
	v_readlane_b32 s60, v255, 11
	s_cbranch_vccnz .LBB0_886
	global_load_dwordx4 v[132:135], v[150:151], off nt
	global_load_dwordx4 v[128:131], v[150:151], off offset:16 nt
	s_mov_b64 s[0:1], 0
	s_branch .LBB0_887

; DI unsigned pk_bf16(float lo, float hi) { const f32x2 v = {lo, hi}; return __builtin_bit_cast(unsigned, __builtin_convertvector(v, bf16x2_t)); }
;     DI void operator()(const f32x4 (&acc)[2][2][4][2], const Unit& u, int wr, int wc, int fr, int fq) const {
;     ...
;                 for (int bj = 0; bj < 2; ++bj) {
;                     float h[8];
;                     if (x) { const f32x4 h0 = *(const f32x4*)(x + ro + bj * 128), h1 = *(const f32x4*)(x + ro + bj * 128 + 4); h[0] = h0[0]; h[1] = h0[1]; h[2] = h0[2]; h[3] = h0[3]; h[4] = h1[0]; h[5] = h1[1]; h[6] = h1[2]; h[7] = h1[3]; }
;                     else res8(*(const u32x4*)(HB + ro + bj * 128), *(const u32x4*)(HLO + ro + bj * 128), h);
;                     const f32x4 a0 = acc[ai][bj][m][0], a1 = acc[ai][bj][m][1];
;                     u32x4 w; w.x = pk_bf16(h[0] * ALPHA + a0[0], h[1] * ALPHA + a0[1]); w.y = pk_bf16(h[2] * ALPHA + a0[2], h[3] * ALPHA + a0[3]);
;                     w.z = pk_bf16(h[4] * ALPHA + a1[0], h[5] * ALPHA + a1[1]); w.w = pk_bf16(h[6] * ALPHA + a1[2], h[7] * ALPHA + a1[3]);
;                     *(u32x4*)(V + ro + bj * 128) = w; } }
.LBB0_889:
	s_waitcnt vmcnt(0)
	v_pk_fma_f32 v[124:125], v[132:133], s[74:75], v[124:125] op_sel_hi:[1,0,1]
	v_pk_fma_f32 v[126:127], v[134:135], s[74:75], v[126:127] op_sel_hi:[1,0,1]
	v_pk_fma_f32 v[120:121], v[128:129], s[74:75], v[120:121] op_sel_hi:[1,0,1]
	v_cvt_pk_bf16_f32 v124, v124, v125
	v_cvt_pk_bf16_f32 v125, v126, v127
	v_cvt_pk_bf16_f32 v126, v120, v121
	v_pk_fma_f32 v[120:121], v[130:131], s[74:75], v[122:123] op_sel_hi:[1,0,1]
	v_lshl_add_u64 v[128:129], v[152:153], 1, s[8:9]
	v_cvt_pk_bf16_f32 v127, v120, v121
	s_and_b64 vcc, exec, s[4:5]
	global_store_dwordx4 v[128:129], v[124:127], off
	s_cbranch_vccnz .LBB0_894
	global_load_dwordx4 v[124:127], v[150:151], off offset:512 nt
	global_load_dwordx4 v[120:123], v[150:151], off offset:528 nt
	s_cbranch_execnz .LBB0_892

; DI unsigned pk_bf16(float lo, float hi) { const f32x2 v = {lo, hi}; return __builtin_bit_cast(unsigned, __builtin_convertvector(v, bf16x2_t)); }
;     DI void operator()(const f32x4 (&acc)[2][2][4][2], const Unit& u, int wr, int wc, int fr, int fq) const {
;     ...
;             for (int m = 0; m < 4; ++m) { const size_t ro = (size_t)(u.orow + ai * 128 + wr * 64 + m * 16 + fr) * 1024 + col0;
; #pragma unroll
;                 for (int bj = 0; bj < 2; ++bj) {
;                     float h[8];
;                     if (x) { const f32x4 h0 = *(const f32x4*)(x + ro + bj * 128), h1 = *(const f32x4*)(x + ro + bj * 128 + 4); h[0] = h0[0]; h[1] = h0[1]; h[2] = h0[2]; h[3] = h0[3]; h[4] = h1[0]; h[5] = h1[1]; h[6] = h1[2]; h[7] = h1[3]; }
;                     else res8(*(const u32x4*)(HB + ro + bj * 128), *(const u32x4*)(HLO + ro + bj * 128), h);
;                     const f32x4 a0 = acc[ai][bj][m][0], a1 = acc[ai][bj][m][1];
;                     u32x4 w; w.x = pk_bf16(h[0] * ALPHA + a0[0], h[1] * ALPHA + a0[1]); w.y = pk_bf16(h[2] * ALPHA + a0[2], h[3] * ALPHA + a0[3]);
;                     w.z = pk_bf16(h[4] * ALPHA + a1[0], h[5] * ALPHA + a1[1]); w.w = pk_bf16(h[6] * ALPHA + a1[2], h[7] * ALPHA + a1[3]);
;                     *(u32x4*)(V + ro + bj * 128) = w; } }
.LBB0_892:
	s_waitcnt vmcnt(1)
	v_pk_fma_f32 v[116:117], v[124:125], s[74:75], v[116:117] op_sel_hi:[1,0,1]
	v_pk_fma_f32 v[118:119], v[126:127], s[74:75], v[118:119] op_sel_hi:[1,0,1]
	s_waitcnt vmcnt(0)
	v_pk_fma_f32 v[112:113], v[120:121], s[74:75], v[112:113] op_sel_hi:[1,0,1]
	v_cvt_pk_bf16_f32 v116, v116, v117
	v_cvt_pk_bf16_f32 v117, v118, v119
	v_cvt_pk_bf16_f32 v118, v112, v113
	v_pk_fma_f32 v[112:113], v[122:123], s[74:75], v[114:115] op_sel_hi:[1,0,1]
	s_and_b64 vcc, exec, s[4:5]
	v_cvt_pk_bf16_f32 v119, v112, v113
	v_add_u32_e32 v112, 16, v144
	v_ashrrev_i32_e32 v113, 31, v112
	v_lshlrev_b64 v[112:113], 10, v[112:113]
	v_lshl_add_u64 v[126:127], v[112:113], 0, v[142:143]
	v_lshl_add_u64 v[124:125], v[126:127], 2, s[18:19]
	global_store_dwordx4 v[128:129], v[116:119], off offset:256
	s_cbranch_vccnz .LBB0_895
	global_load_dwordx4 v[116:119], v[124:125], off nt
	global_load_dwordx4 v[112:115], v[124:125], off offset:16 nt
	s_mov_b64 s[0:1], 0
	s_branch .LBB0_896

; DI unsigned pk_bf16(float lo, float hi) { const f32x2 v = {lo, hi}; return __builtin_bit_cast(unsigned, __builtin_convertvector(v, bf16x2_t)); }
;     DI void operator()(const f32x4 (&acc)[2][2][4][2], const Unit& u, int wr, int wc, int fr, int fq) const {
;     ...
;                 for (int bj = 0; bj < 2; ++bj) {
;                     float h[8];
;                     if (x) { const f32x4 h0 = *(const f32x4*)(x + ro + bj * 128), h1 = *(const f32x4*)(x + ro + bj * 128 + 4); h[0] = h0[0]; h[1] = h0[1]; h[2] = h0[2]; h[3] = h0[3]; h[4] = h1[0]; h[5] = h1[1]; h[6] = h1[2]; h[7] = h1[3]; }
;                     else res8(*(const u32x4*)(HB + ro + bj * 128), *(const u32x4*)(HLO + ro + bj * 128), h);
;                     const f32x4 a0 = acc[ai][bj][m][0], a1 = acc[ai][bj][m][1];
;                     u32x4 w; w.x = pk_bf16(h[0] * ALPHA + a0[0], h[1] * ALPHA + a0[1]); w.y = pk_bf16(h[2] * ALPHA + a0[2], h[3] * ALPHA + a0[3]);
;                     w.z = pk_bf16(h[4] * ALPHA + a1[0], h[5] * ALPHA + a1[1]); w.w = pk_bf16(h[6] * ALPHA + a1[2], h[7] * ALPHA + a1[3]);
;                     *(u32x4*)(V + ro + bj * 128) = w; } }
.LBB0_898:
	s_waitcnt vmcnt(1)
	v_pk_fma_f32 v[108:109], v[116:117], s[74:75], v[108:109] op_sel_hi:[1,0,1]
	v_pk_fma_f32 v[110:111], v[118:119], s[74:75], v[110:111] op_sel_hi:[1,0,1]
	s_waitcnt vmcnt(0)
	v_pk_fma_f32 v[104:105], v[112:113], s[74:75], v[104:105] op_sel_hi:[1,0,1]
	v_cvt_pk_bf16_f32 v108, v108, v109
	v_cvt_pk_bf16_f32 v109, v110, v111
	v_cvt_pk_bf16_f32 v110, v104, v105
	v_pk_fma_f32 v[104:105], v[114:115], s[74:75], v[106:107] op_sel_hi:[1,0,1]
	v_lshl_add_u64 v[112:113], v[126:127], 1, s[8:9]
	v_cvt_pk_bf16_f32 v111, v104, v105
	s_and_b64 vcc, exec, s[4:5]
	global_store_dwordx4 v[112:113], v[108:111], off
	s_cbranch_vccnz .LBB0_903
	global_load_dwordx4 v[108:111], v[124:125], off offset:512 nt
	global_load_dwordx4 v[104:107], v[124:125], off offset:528 nt
	s_cbranch_execnz .LBB0_901

; DI unsigned pk_bf16(float lo, float hi) { const f32x2 v = {lo, hi}; return __builtin_bit_cast(unsigned, __builtin_convertvector(v, bf16x2_t)); }
;     DI void operator()(const f32x4 (&acc)[2][2][4][2], const Unit& u, int wr, int wc, int fr, int fq) const {
;     ...
;             for (int m = 0; m < 4; ++m) { const size_t ro = (size_t)(u.orow + ai * 128 + wr * 64 + m * 16 + fr) * 1024 + col0;
; #pragma unroll
;                 for (int bj = 0; bj < 2; ++bj) {
;                     float h[8];
;                     if (x) { const f32x4 h0 = *(const f32x4*)(x + ro + bj * 128), h1 = *(const f32x4*)(x + ro + bj * 128 + 4); h[0] = h0[0]; h[1] = h0[1]; h[2] = h0[2]; h[3] = h0[3]; h[4] = h1[0]; h[5] = h1[1]; h[6] = h1[2]; h[7] = h1[3]; }
;                     else res8(*(const u32x4*)(HB + ro + bj * 128), *(const u32x4*)(HLO + ro + bj * 128), h);
;                     const f32x4 a0 = acc[ai][bj][m][0], a1 = acc[ai][bj][m][1];
;                     u32x4 w; w.x = pk_bf16(h[0] * ALPHA + a0[0], h[1] * ALPHA + a0[1]); w.y = pk_bf16(h[2] * ALPHA + a0[2], h[3] * ALPHA + a0[3]);
;                     w.z = pk_bf16(h[4] * ALPHA + a1[0], h[5] * ALPHA + a1[1]); w.w = pk_bf16(h[6] * ALPHA + a1[2], h[7] * ALPHA + a1[3]);
;                     *(u32x4*)(V + ro + bj * 128) = w; } }
.LBB0_901:
	s_waitcnt vmcnt(1)
	v_pk_fma_f32 v[100:101], v[108:109], s[74:75], v[100:101] op_sel_hi:[1,0,1]
	v_pk_fma_f32 v[102:103], v[110:111], s[74:75], v[102:103] op_sel_hi:[1,0,1]
	s_waitcnt vmcnt(0)
	v_pk_fma_f32 v[96:97], v[104:105], s[74:75], v[96:97] op_sel_hi:[1,0,1]
	v_cvt_pk_bf16_f32 v100, v100, v101
	v_cvt_pk_bf16_f32 v101, v102, v103
	v_cvt_pk_bf16_f32 v102, v96, v97
	v_pk_fma_f32 v[96:97], v[106:107], s[74:75], v[98:99] op_sel_hi:[1,0,1]
	s_and_b64 vcc, exec, s[4:5]
	v_cvt_pk_bf16_f32 v103, v96, v97
	v_add_u32_e32 v96, 32, v144
	v_ashrrev_i32_e32 v97, 31, v96
	v_lshlrev_b64 v[96:97], 10, v[96:97]
	v_lshl_add_u64 v[110:111], v[96:97], 0, v[142:143]
	v_lshl_add_u64 v[108:109], v[110:111], 2, s[18:19]
	global_store_dwordx4 v[112:113], v[100:103], off offset:256
	s_cbranch_vccnz .LBB0_904
	global_load_dwordx4 v[100:103], v[108:109], off nt
	global_load_dwordx4 v[96:99], v[108:109], off offset:16 nt
	s_mov_b64 s[0:1], 0
	s_branch .LBB0_905

; DI unsigned pk_bf16(float lo, float hi) { const f32x2 v = {lo, hi}; return __builtin_bit_cast(unsigned, __builtin_convertvector(v, bf16x2_t)); }
;     DI void operator()(const f32x4 (&acc)[2][2][4][2], const Unit& u, int wr, int wc, int fr, int fq) const {
;     ...
;                 for (int bj = 0; bj < 2; ++bj) {
;                     float h[8];
;                     if (x) { const f32x4 h0 = *(const f32x4*)(x + ro + bj * 128), h1 = *(const f32x4*)(x + ro + bj * 128 + 4); h[0] = h0[0]; h[1] = h0[1]; h[2] = h0[2]; h[3] = h0[3]; h[4] = h1[0]; h[5] = h1[1]; h[6] = h1[2]; h[7] = h1[3]; }
;                     else res8(*(const u32x4*)(HB + ro + bj * 128), *(const u32x4*)(HLO + ro + bj * 128), h);
;                     const f32x4 a0 = acc[ai][bj][m][0], a1 = acc[ai][bj][m][1];
;                     u32x4 w; w.x = pk_bf16(h[0] * ALPHA + a0[0], h[1] * ALPHA + a0[1]); w.y = pk_bf16(h[2] * ALPHA + a0[2], h[3] * ALPHA + a0[3]);
;                     w.z = pk_bf16(h[4] * ALPHA + a1[0], h[5] * ALPHA + a1[1]); w.w = pk_bf16(h[6] * ALPHA + a1[2], h[7] * ALPHA + a1[3]);
;                     *(u32x4*)(V + ro + bj * 128) = w; } }
.LBB0_907:
	s_waitcnt vmcnt(1)
	v_pk_fma_f32 v[92:93], v[100:101], s[74:75], v[92:93] op_sel_hi:[1,0,1]
	v_pk_fma_f32 v[94:95], v[102:103], s[74:75], v[94:95] op_sel_hi:[1,0,1]
	s_waitcnt vmcnt(0)
	v_pk_fma_f32 v[88:89], v[96:97], s[74:75], v[88:89] op_sel_hi:[1,0,1]
	v_cvt_pk_bf16_f32 v92, v92, v93
	v_cvt_pk_bf16_f32 v93, v94, v95
	v_cvt_pk_bf16_f32 v94, v88, v89
	v_pk_fma_f32 v[88:89], v[98:99], s[74:75], v[90:91] op_sel_hi:[1,0,1]
	v_lshl_add_u64 v[96:97], v[110:111], 1, s[8:9]
	v_cvt_pk_bf16_f32 v95, v88, v89
	s_and_b64 vcc, exec, s[4:5]
	global_store_dwordx4 v[96:97], v[92:95], off
	s_cbranch_vccnz .LBB0_912
	global_load_dwordx4 v[92:95], v[108:109], off offset:512 nt
	global_load_dwordx4 v[88:91], v[108:109], off offset:528 nt
	s_cbranch_execnz .LBB0_910

; DI unsigned pk_bf16(float lo, float hi) { const f32x2 v = {lo, hi}; return __builtin_bit_cast(unsigned, __builtin_convertvector(v, bf16x2_t)); }
;     DI void operator()(const f32x4 (&acc)[2][2][4][2], const Unit& u, int wr, int wc, int fr, int fq) const {
;     ...
;             for (int m = 0; m < 4; ++m) { const size_t ro = (size_t)(u.orow + ai * 128 + wr * 64 + m * 16 + fr) * 1024 + col0;
; #pragma unroll
;                 for (int bj = 0; bj < 2; ++bj) {
;                     float h[8];
;                     if (x) { const f32x4 h0 = *(const f32x4*)(x + ro + bj * 128), h1 = *(const f32x4*)(x + ro + bj * 128 + 4); h[0] = h0[0]; h[1] = h0[1]; h[2] = h0[2]; h[3] = h0[3]; h[4] = h1[0]; h[5] = h1[1]; h[6] = h1[2]; h[7] = h1[3]; }
;                     else res8(*(const u32x4*)(HB + ro + bj * 128), *(const u32x4*)(HLO + ro + bj * 128), h);
;                     const f32x4 a0 = acc[ai][bj][m][0], a1 = acc[ai][bj][m][1];
;                     u32x4 w; w.x = pk_bf16(h[0] * ALPHA + a0[0], h[1] * ALPHA + a0[1]); w.y = pk_bf16(h[2] * ALPHA + a0[2], h[3] * ALPHA + a0[3]);
;                     w.z = pk_bf16(h[4] * ALPHA + a1[0], h[5] * ALPHA + a1[1]); w.w = pk_bf16(h[6] * ALPHA + a1[2], h[7] * ALPHA + a1[3]);
;                     *(u32x4*)(V + ro + bj * 128) = w; } }
.LBB0_910:
	s_waitcnt vmcnt(1)
	v_pk_fma_f32 v[84:85], v[92:93], s[74:75], v[84:85] op_sel_hi:[1,0,1]
	v_pk_fma_f32 v[86:87], v[94:95], s[74:75], v[86:87] op_sel_hi:[1,0,1]
	s_waitcnt vmcnt(0)
	v_pk_fma_f32 v[80:81], v[88:89], s[74:75], v[80:81] op_sel_hi:[1,0,1]
	v_cvt_pk_bf16_f32 v84, v84, v85
	v_cvt_pk_bf16_f32 v85, v86, v87
	v_cvt_pk_bf16_f32 v86, v80, v81
	v_pk_fma_f32 v[80:81], v[90:91], s[74:75], v[82:83] op_sel_hi:[1,0,1]
	s_and_b64 vcc, exec, s[4:5]
	v_cvt_pk_bf16_f32 v87, v80, v81
	v_add_u32_e32 v80, 48, v144
	v_ashrrev_i32_e32 v81, 31, v80
	v_lshlrev_b64 v[80:81], 10, v[80:81]
	v_lshl_add_u64 v[94:95], v[80:81], 0, v[142:143]
	v_lshl_add_u64 v[92:93], v[94:95], 2, s[18:19]
	global_store_dwordx4 v[96:97], v[84:87], off offset:256
	s_cbranch_vccnz .LBB0_913
	global_load_dwordx4 v[84:87], v[92:93], off nt
	global_load_dwordx4 v[80:83], v[92:93], off offset:16 nt
	s_mov_b64 s[0:1], 0
	s_branch .LBB0_914

; DI unsigned pk_bf16(float lo, float hi) { const f32x2 v = {lo, hi}; return __builtin_bit_cast(unsigned, __builtin_convertvector(v, bf16x2_t)); }
;     DI void operator()(const f32x4 (&acc)[2][2][4][2], const Unit& u, int wr, int wc, int fr, int fq) const {
;     ...
;                 for (int bj = 0; bj < 2; ++bj) {
;                     float h[8];
;                     if (x) { const f32x4 h0 = *(const f32x4*)(x + ro + bj * 128), h1 = *(const f32x4*)(x + ro + bj * 128 + 4); h[0] = h0[0]; h[1] = h0[1]; h[2] = h0[2]; h[3] = h0[3]; h[4] = h1[0]; h[5] = h1[1]; h[6] = h1[2]; h[7] = h1[3]; }
;                     else res8(*(const u32x4*)(HB + ro + bj * 128), *(const u32x4*)(HLO + ro + bj * 128), h);
;                     const f32x4 a0 = acc[ai][bj][m][0], a1 = acc[ai][bj][m][1];
;                     u32x4 w; w.x = pk_bf16(h[0] * ALPHA + a0[0], h[1] * ALPHA + a0[1]); w.y = pk_bf16(h[2] * ALPHA + a0[2], h[3] * ALPHA + a0[3]);
;                     w.z = pk_bf16(h[4] * ALPHA + a1[0], h[5] * ALPHA + a1[1]); w.w = pk_bf16(h[6] * ALPHA + a1[2], h[7] * ALPHA + a1[3]);
;                     *(u32x4*)(V + ro + bj * 128) = w; } }
.LBB0_916:
	s_waitcnt vmcnt(1)
	v_pk_fma_f32 v[76:77], v[84:85], s[74:75], v[76:77] op_sel_hi:[1,0,1]
	v_pk_fma_f32 v[78:79], v[86:87], s[74:75], v[78:79] op_sel_hi:[1,0,1]
	s_waitcnt vmcnt(0)
	v_pk_fma_f32 v[72:73], v[80:81], s[74:75], v[72:73] op_sel_hi:[1,0,1]
	v_cvt_pk_bf16_f32 v76, v76, v77
	v_cvt_pk_bf16_f32 v77, v78, v79
	v_cvt_pk_bf16_f32 v78, v72, v73
	v_pk_fma_f32 v[72:73], v[82:83], s[74:75], v[74:75] op_sel_hi:[1,0,1]
	v_lshl_add_u64 v[80:81], v[94:95], 1, s[8:9]
	v_cvt_pk_bf16_f32 v79, v72, v73
	s_and_b64 vcc, exec, s[4:5]
	global_store_dwordx4 v[80:81], v[76:79], off
	s_cbranch_vccnz .LBB0_921
	global_load_dwordx4 v[76:79], v[92:93], off offset:512 nt
	global_load_dwordx4 v[72:75], v[92:93], off offset:528 nt
	s_cbranch_execnz .LBB0_919

; DI unsigned pk_bf16(float lo, float hi) { const f32x2 v = {lo, hi}; return __builtin_bit_cast(unsigned, __builtin_convertvector(v, bf16x2_t)); }
;     DI void operator()(const f32x4 (&acc)[2][2][4][2], const Unit& u, int wr, int wc, int fr, int fq) const {
;     ...
;             for (int m = 0; m < 4; ++m) { const size_t ro = (size_t)(u.orow + ai * 128 + wr * 64 + m * 16 + fr) * 1024 + col0;
; #pragma unroll
;                 for (int bj = 0; bj < 2; ++bj) {
;                     float h[8];
;                     if (x) { const f32x4 h0 = *(const f32x4*)(x + ro + bj * 128), h1 = *(const f32x4*)(x + ro + bj * 128 + 4); h[0] = h0[0]; h[1] = h0[1]; h[2] = h0[2]; h[3] = h0[3]; h[4] = h1[0]; h[5] = h1[1]; h[6] = h1[2]; h[7] = h1[3]; }
;                     else res8(*(const u32x4*)(HB + ro + bj * 128), *(const u32x4*)(HLO + ro + bj * 128), h);
;                     const f32x4 a0 = acc[ai][bj][m][0], a1 = acc[ai][bj][m][1];
;                     u32x4 w; w.x = pk_bf16(h[0] * ALPHA + a0[0], h[1] * ALPHA + a0[1]); w.y = pk_bf16(h[2] * ALPHA + a0[2], h[3] * ALPHA + a0[3]);
;                     w.z = pk_bf16(h[4] * ALPHA + a1[0], h[5] * ALPHA + a1[1]); w.w = pk_bf16(h[6] * ALPHA + a1[2], h[7] * ALPHA + a1[3]);
;                     *(u32x4*)(V + ro + bj * 128) = w; } }
.LBB0_919:
	s_waitcnt vmcnt(1)
	v_pk_fma_f32 v[68:69], v[76:77], s[74:75], v[68:69] op_sel_hi:[1,0,1]
	v_pk_fma_f32 v[70:71], v[78:79], s[74:75], v[70:71] op_sel_hi:[1,0,1]
	s_waitcnt vmcnt(0)
	v_pk_fma_f32 v[64:65], v[72:73], s[74:75], v[64:65] op_sel_hi:[1,0,1]
	v_cvt_pk_bf16_f32 v68, v68, v69
	v_cvt_pk_bf16_f32 v69, v70, v71
	v_cvt_pk_bf16_f32 v70, v64, v65
	v_pk_fma_f32 v[64:65], v[74:75], s[74:75], v[66:67] op_sel_hi:[1,0,1]
	s_and_b64 vcc, exec, s[4:5]
	v_cvt_pk_bf16_f32 v71, v64, v65
	v_add_u32_e32 v64, 0x80, v144
	v_ashrrev_i32_e32 v65, 31, v64
	v_lshlrev_b64 v[64:65], 10, v[64:65]
	v_lshl_add_u64 v[78:79], v[64:65], 0, v[142:143]
	v_lshl_add_u64 v[76:77], v[78:79], 2, s[18:19]
	global_store_dwordx4 v[80:81], v[68:71], off offset:256
	s_cbranch_vccnz .LBB0_922
	global_load_dwordx4 v[68:71], v[76:77], off nt
	global_load_dwordx4 v[64:67], v[76:77], off offset:16 nt
	s_mov_b64 s[0:1], 0
	s_branch .LBB0_923

; DI unsigned pk_bf16(float lo, float hi) { const f32x2 v = {lo, hi}; return __builtin_bit_cast(unsigned, __builtin_convertvector(v, bf16x2_t)); }
;     DI void operator()(const f32x4 (&acc)[2][2][4][2], const Unit& u, int wr, int wc, int fr, int fq) const {
;     ...
;                 for (int bj = 0; bj < 2; ++bj) {
;                     float h[8];
;                     if (x) { const f32x4 h0 = *(const f32x4*)(x + ro + bj * 128), h1 = *(const f32x4*)(x + ro + bj * 128 + 4); h[0] = h0[0]; h[1] = h0[1]; h[2] = h0[2]; h[3] = h0[3]; h[4] = h1[0]; h[5] = h1[1]; h[6] = h1[2]; h[7] = h1[3]; }
;                     else res8(*(const u32x4*)(HB + ro + bj * 128), *(const u32x4*)(HLO + ro + bj * 128), h);
;                     const f32x4 a0 = acc[ai][bj][m][0], a1 = acc[ai][bj][m][1];
;                     u32x4 w; w.x = pk_bf16(h[0] * ALPHA + a0[0], h[1] * ALPHA + a0[1]); w.y = pk_bf16(h[2] * ALPHA + a0[2], h[3] * ALPHA + a0[3]);
;                     w.z = pk_bf16(h[4] * ALPHA + a1[0], h[5] * ALPHA + a1[1]); w.w = pk_bf16(h[6] * ALPHA + a1[2], h[7] * ALPHA + a1[3]);
;                     *(u32x4*)(V + ro + bj * 128) = w; } }
.LBB0_925:
	s_waitcnt vmcnt(1)
	v_pk_fma_f32 v[60:61], v[68:69], s[74:75], v[60:61] op_sel_hi:[1,0,1]
	v_pk_fma_f32 v[62:63], v[70:71], s[74:75], v[62:63] op_sel_hi:[1,0,1]
	s_waitcnt vmcnt(0)
	v_pk_fma_f32 v[56:57], v[64:65], s[74:75], v[56:57] op_sel_hi:[1,0,1]
	v_cvt_pk_bf16_f32 v60, v60, v61
	v_cvt_pk_bf16_f32 v61, v62, v63
	v_cvt_pk_bf16_f32 v62, v56, v57
	v_pk_fma_f32 v[56:57], v[66:67], s[74:75], v[58:59] op_sel_hi:[1,0,1]
	v_lshl_add_u64 v[64:65], v[78:79], 1, s[8:9]
	v_cvt_pk_bf16_f32 v63, v56, v57
	s_and_b64 vcc, exec, s[4:5]
	global_store_dwordx4 v[64:65], v[60:63], off
	s_cbranch_vccnz .LBB0_930
	global_load_dwordx4 v[60:63], v[76:77], off offset:512 nt
	global_load_dwordx4 v[56:59], v[76:77], off offset:528 nt
	s_cbranch_execnz .LBB0_928

; DI unsigned pk_bf16(float lo, float hi) { const f32x2 v = {lo, hi}; return __builtin_bit_cast(unsigned, __builtin_convertvector(v, bf16x2_t)); }
;     DI void operator()(const f32x4 (&acc)[2][2][4][2], const Unit& u, int wr, int wc, int fr, int fq) const {
;     ...
;             for (int m = 0; m < 4; ++m) { const size_t ro = (size_t)(u.orow + ai * 128 + wr * 64 + m * 16 + fr) * 1024 + col0;
; #pragma unroll
;                 for (int bj = 0; bj < 2; ++bj) {
;                     float h[8];
;                     if (x) { const f32x4 h0 = *(const f32x4*)(x + ro + bj * 128), h1 = *(const f32x4*)(x + ro + bj * 128 + 4); h[0] = h0[0]; h[1] = h0[1]; h[2] = h0[2]; h[3] = h0[3]; h[4] = h1[0]; h[5] = h1[1]; h[6] = h1[2]; h[7] = h1[3]; }
;                     else res8(*(const u32x4*)(HB + ro + bj * 128), *(const u32x4*)(HLO + ro + bj * 128), h);
;                     const f32x4 a0 = acc[ai][bj][m][0], a1 = acc[ai][bj][m][1];
;                     u32x4 w; w.x = pk_bf16(h[0] * ALPHA + a0[0], h[1] * ALPHA + a0[1]); w.y = pk_bf16(h[2] * ALPHA + a0[2], h[3] * ALPHA + a0[3]);
;                     w.z = pk_bf16(h[4] * ALPHA + a1[0], h[5] * ALPHA + a1[1]); w.w = pk_bf16(h[6] * ALPHA + a1[2], h[7] * ALPHA + a1[3]);
;                     *(u32x4*)(V + ro + bj * 128) = w; } }
.LBB0_928:
	s_waitcnt vmcnt(1)
	v_pk_fma_f32 v[52:53], v[60:61], s[74:75], v[52:53] op_sel_hi:[1,0,1]
	v_pk_fma_f32 v[54:55], v[62:63], s[74:75], v[54:55] op_sel_hi:[1,0,1]
	s_waitcnt vmcnt(0)
	v_pk_fma_f32 v[48:49], v[56:57], s[74:75], v[48:49] op_sel_hi:[1,0,1]
	v_cvt_pk_bf16_f32 v52, v52, v53
	v_cvt_pk_bf16_f32 v53, v54, v55
	v_cvt_pk_bf16_f32 v54, v48, v49
	v_pk_fma_f32 v[48:49], v[58:59], s[74:75], v[50:51] op_sel_hi:[1,0,1]
	s_and_b64 vcc, exec, s[4:5]
	v_cvt_pk_bf16_f32 v55, v48, v49
	v_add_u32_e32 v48, 0x90, v144
	v_ashrrev_i32_e32 v49, 31, v48
	v_lshlrev_b64 v[48:49], 10, v[48:49]
	v_lshl_add_u64 v[62:63], v[48:49], 0, v[142:143]
	v_lshl_add_u64 v[60:61], v[62:63], 2, s[18:19]
	global_store_dwordx4 v[64:65], v[52:55], off offset:256
	s_cbranch_vccnz .LBB0_931
	global_load_dwordx4 v[52:55], v[60:61], off nt
	global_load_dwordx4 v[48:51], v[60:61], off offset:16 nt
	s_mov_b64 s[0:1], 0
	s_branch .LBB0_932

; DI unsigned pk_bf16(float lo, float hi) { const f32x2 v = {lo, hi}; return __builtin_bit_cast(unsigned, __builtin_convertvector(v, bf16x2_t)); }
;     DI void operator()(const f32x4 (&acc)[2][2][4][2], const Unit& u, int wr, int wc, int fr, int fq) const {
;     ...
;                 for (int bj = 0; bj < 2; ++bj) {
;                     float h[8];
;                     if (x) { const f32x4 h0 = *(const f32x4*)(x + ro + bj * 128), h1 = *(const f32x4*)(x + ro + bj * 128 + 4); h[0] = h0[0]; h[1] = h0[1]; h[2] = h0[2]; h[3] = h0[3]; h[4] = h1[0]; h[5] = h1[1]; h[6] = h1[2]; h[7] = h1[3]; }
;                     else res8(*(const u32x4*)(HB + ro + bj * 128), *(const u32x4*)(HLO + ro + bj * 128), h);
;                     const f32x4 a0 = acc[ai][bj][m][0], a1 = acc[ai][bj][m][1];
;                     u32x4 w; w.x = pk_bf16(h[0] * ALPHA + a0[0], h[1] * ALPHA + a0[1]); w.y = pk_bf16(h[2] * ALPHA + a0[2], h[3] * ALPHA + a0[3]);
;                     w.z = pk_bf16(h[4] * ALPHA + a1[0], h[5] * ALPHA + a1[1]); w.w = pk_bf16(h[6] * ALPHA + a1[2], h[7] * ALPHA + a1[3]);
;                     *(u32x4*)(V + ro + bj * 128) = w; } }
.LBB0_934:
	s_waitcnt vmcnt(1)
	v_pk_fma_f32 v[44:45], v[52:53], s[74:75], v[44:45] op_sel_hi:[1,0,1]
	v_pk_fma_f32 v[46:47], v[54:55], s[74:75], v[46:47] op_sel_hi:[1,0,1]
	s_waitcnt vmcnt(0)
	v_pk_fma_f32 v[40:41], v[48:49], s[74:75], v[40:41] op_sel_hi:[1,0,1]
	v_cvt_pk_bf16_f32 v44, v44, v45
	v_cvt_pk_bf16_f32 v45, v46, v47
	v_cvt_pk_bf16_f32 v46, v40, v41
	v_pk_fma_f32 v[40:41], v[50:51], s[74:75], v[42:43] op_sel_hi:[1,0,1]
	v_lshl_add_u64 v[48:49], v[62:63], 1, s[8:9]
	v_cvt_pk_bf16_f32 v47, v40, v41
	s_and_b64 vcc, exec, s[4:5]
	global_store_dwordx4 v[48:49], v[44:47], off
	s_cbranch_vccnz .LBB0_939
	global_load_dwordx4 v[44:47], v[60:61], off offset:512 nt
	global_load_dwordx4 v[40:43], v[60:61], off offset:528 nt
	s_cbranch_execnz .LBB0_937

; DI unsigned pk_bf16(float lo, float hi) { const f32x2 v = {lo, hi}; return __builtin_bit_cast(unsigned, __builtin_convertvector(v, bf16x2_t)); }
;     DI void operator()(const f32x4 (&acc)[2][2][4][2], const Unit& u, int wr, int wc, int fr, int fq) const {
;     ...
;             for (int m = 0; m < 4; ++m) { const size_t ro = (size_t)(u.orow + ai * 128 + wr * 64 + m * 16 + fr) * 1024 + col0;
; #pragma unroll
;                 for (int bj = 0; bj < 2; ++bj) {
;                     float h[8];
;                     if (x) { const f32x4 h0 = *(const f32x4*)(x + ro + bj * 128), h1 = *(const f32x4*)(x + ro + bj * 128 + 4); h[0] = h0[0]; h[1] = h0[1]; h[2] = h0[2]; h[3] = h0[3]; h[4] = h1[0]; h[5] = h1[1]; h[6] = h1[2]; h[7] = h1[3]; }
;                     else res8(*(const u32x4*)(HB + ro + bj * 128), *(const u32x4*)(HLO + ro + bj * 128), h);
;                     const f32x4 a0 = acc[ai][bj][m][0], a1 = acc[ai][bj][m][1];
;                     u32x4 w; w.x = pk_bf16(h[0] * ALPHA + a0[0], h[1] * ALPHA + a0[1]); w.y = pk_bf16(h[2] * ALPHA + a0[2], h[3] * ALPHA + a0[3]);
;                     w.z = pk_bf16(h[4] * ALPHA + a1[0], h[5] * ALPHA + a1[1]); w.w = pk_bf16(h[6] * ALPHA + a1[2], h[7] * ALPHA + a1[3]);
;                     *(u32x4*)(V + ro + bj * 128) = w; } }
.LBB0_937:
	s_waitcnt vmcnt(1)
	v_pk_fma_f32 v[36:37], v[44:45], s[74:75], v[36:37] op_sel_hi:[1,0,1]
	v_pk_fma_f32 v[38:39], v[46:47], s[74:75], v[38:39] op_sel_hi:[1,0,1]
	s_waitcnt vmcnt(0)
	v_pk_fma_f32 v[32:33], v[40:41], s[74:75], v[32:33] op_sel_hi:[1,0,1]
	v_cvt_pk_bf16_f32 v36, v36, v37
	v_cvt_pk_bf16_f32 v37, v38, v39
	v_cvt_pk_bf16_f32 v38, v32, v33
	v_pk_fma_f32 v[32:33], v[42:43], s[74:75], v[34:35] op_sel_hi:[1,0,1]
	s_and_b64 vcc, exec, s[4:5]
	v_cvt_pk_bf16_f32 v39, v32, v33
	v_add_u32_e32 v32, 0xa0, v144
	v_ashrrev_i32_e32 v33, 31, v32
	v_lshlrev_b64 v[32:33], 10, v[32:33]
	v_lshl_add_u64 v[46:47], v[32:33], 0, v[142:143]
	v_lshl_add_u64 v[44:45], v[46:47], 2, s[18:19]
	global_store_dwordx4 v[48:49], v[36:39], off offset:256
	s_cbranch_vccnz .LBB0_940
	global_load_dwordx4 v[36:39], v[44:45], off nt
	global_load_dwordx4 v[32:35], v[44:45], off offset:16 nt
	s_mov_b64 s[0:1], 0
	s_branch .LBB0_941

; DI unsigned pk_bf16(float lo, float hi) { const f32x2 v = {lo, hi}; return __builtin_bit_cast(unsigned, __builtin_convertvector(v, bf16x2_t)); }
;     DI void operator()(const f32x4 (&acc)[2][2][4][2], const Unit& u, int wr, int wc, int fr, int fq) const {
;     ...
;                 for (int bj = 0; bj < 2; ++bj) {
;                     float h[8];
;                     if (x) { const f32x4 h0 = *(const f32x4*)(x + ro + bj * 128), h1 = *(const f32x4*)(x + ro + bj * 128 + 4); h[0] = h0[0]; h[1] = h0[1]; h[2] = h0[2]; h[3] = h0[3]; h[4] = h1[0]; h[5] = h1[1]; h[6] = h1[2]; h[7] = h1[3]; }
;                     else res8(*(const u32x4*)(HB + ro + bj * 128), *(const u32x4*)(HLO + ro + bj * 128), h);
;                     const f32x4 a0 = acc[ai][bj][m][0], a1 = acc[ai][bj][m][1];
;                     u32x4 w; w.x = pk_bf16(h[0] * ALPHA + a0[0], h[1] * ALPHA + a0[1]); w.y = pk_bf16(h[2] * ALPHA + a0[2], h[3] * ALPHA + a0[3]);
;                     w.z = pk_bf16(h[4] * ALPHA + a1[0], h[5] * ALPHA + a1[1]); w.w = pk_bf16(h[6] * ALPHA + a1[2], h[7] * ALPHA + a1[3]);
;                     *(u32x4*)(V + ro + bj * 128) = w; } }
.LBB0_943:
	s_waitcnt vmcnt(1)
	v_pk_fma_f32 v[28:29], v[36:37], s[74:75], v[28:29] op_sel_hi:[1,0,1]
	v_pk_fma_f32 v[30:31], v[38:39], s[74:75], v[30:31] op_sel_hi:[1,0,1]
	s_waitcnt vmcnt(0)
	v_pk_fma_f32 v[24:25], v[32:33], s[74:75], v[24:25] op_sel_hi:[1,0,1]
	v_cvt_pk_bf16_f32 v28, v28, v29
	v_cvt_pk_bf16_f32 v29, v30, v31
	v_cvt_pk_bf16_f32 v30, v24, v25
	v_pk_fma_f32 v[24:25], v[34:35], s[74:75], v[26:27] op_sel_hi:[1,0,1]
	v_lshl_add_u64 v[32:33], v[46:47], 1, s[8:9]
	v_cvt_pk_bf16_f32 v31, v24, v25
	s_and_b64 vcc, exec, s[4:5]
	global_store_dwordx4 v[32:33], v[28:31], off
	s_cbranch_vccnz .LBB0_948
	global_load_dwordx4 v[28:31], v[44:45], off offset:512 nt
	global_load_dwordx4 v[24:27], v[44:45], off offset:528 nt
	s_cbranch_execnz .LBB0_946

; DI unsigned pk_bf16(float lo, float hi) { const f32x2 v = {lo, hi}; return __builtin_bit_cast(unsigned, __builtin_convertvector(v, bf16x2_t)); }
;     DI void operator()(const f32x4 (&acc)[2][2][4][2], const Unit& u, int wr, int wc, int fr, int fq) const {
;     ...
;             for (int m = 0; m < 4; ++m) { const size_t ro = (size_t)(u.orow + ai * 128 + wr * 64 + m * 16 + fr) * 1024 + col0;
; #pragma unroll
;                 for (int bj = 0; bj < 2; ++bj) {
;                     float h[8];
;                     if (x) { const f32x4 h0 = *(const f32x4*)(x + ro + bj * 128), h1 = *(const f32x4*)(x + ro + bj * 128 + 4); h[0] = h0[0]; h[1] = h0[1]; h[2] = h0[2]; h[3] = h0[3]; h[4] = h1[0]; h[5] = h1[1]; h[6] = h1[2]; h[7] = h1[3]; }
;                     else res8(*(const u32x4*)(HB + ro + bj * 128), *(const u32x4*)(HLO + ro + bj * 128), h);
;                     const f32x4 a0 = acc[ai][bj][m][0], a1 = acc[ai][bj][m][1];
;                     u32x4 w; w.x = pk_bf16(h[0] * ALPHA + a0[0], h[1] * ALPHA + a0[1]); w.y = pk_bf16(h[2] * ALPHA + a0[2], h[3] * ALPHA + a0[3]);
;                     w.z = pk_bf16(h[4] * ALPHA + a1[0], h[5] * ALPHA + a1[1]); w.w = pk_bf16(h[6] * ALPHA + a1[2], h[7] * ALPHA + a1[3]);
;                     *(u32x4*)(V + ro + bj * 128) = w; } }
.LBB0_946:
	s_waitcnt vmcnt(1)
	v_pk_fma_f32 v[20:21], v[28:29], s[74:75], v[20:21] op_sel_hi:[1,0,1]
	v_pk_fma_f32 v[22:23], v[30:31], s[74:75], v[22:23] op_sel_hi:[1,0,1]
	s_waitcnt vmcnt(0)
	v_pk_fma_f32 v[16:17], v[24:25], s[74:75], v[16:17] op_sel_hi:[1,0,1]
	v_cvt_pk_bf16_f32 v20, v20, v21
	v_cvt_pk_bf16_f32 v21, v22, v23
	v_cvt_pk_bf16_f32 v22, v16, v17
	v_pk_fma_f32 v[16:17], v[26:27], s[74:75], v[18:19] op_sel_hi:[1,0,1]
	s_and_b64 vcc, exec, s[4:5]
	v_cvt_pk_bf16_f32 v23, v16, v17
	v_add_u32_e32 v16, 0xb0, v144
	v_ashrrev_i32_e32 v17, 31, v16
	v_lshlrev_b64 v[16:17], 10, v[16:17]
	v_lshl_add_u64 v[30:31], v[16:17], 0, v[142:143]
	v_lshl_add_u64 v[28:29], v[30:31], 2, s[18:19]
	global_store_dwordx4 v[32:33], v[20:23], off offset:256
	s_cbranch_vccnz .LBB0_949
	global_load_dwordx4 v[20:23], v[28:29], off nt
	global_load_dwordx4 v[16:19], v[28:29], off offset:16 nt
	s_mov_b64 s[0:1], 0
	s_branch .LBB0_950

; DI unsigned pk_bf16(float lo, float hi) { const f32x2 v = {lo, hi}; return __builtin_bit_cast(unsigned, __builtin_convertvector(v, bf16x2_t)); }
;     DI void operator()(const f32x4 (&acc)[2][2][4][2], const Unit& u, int wr, int wc, int fr, int fq) const {
;     ...
;                 for (int bj = 0; bj < 2; ++bj) {
;                     float h[8];
;                     if (x) { const f32x4 h0 = *(const f32x4*)(x + ro + bj * 128), h1 = *(const f32x4*)(x + ro + bj * 128 + 4); h[0] = h0[0]; h[1] = h0[1]; h[2] = h0[2]; h[3] = h0[3]; h[4] = h1[0]; h[5] = h1[1]; h[6] = h1[2]; h[7] = h1[3]; }
;                     else res8(*(const u32x4*)(HB + ro + bj * 128), *(const u32x4*)(HLO + ro + bj * 128), h);
;                     const f32x4 a0 = acc[ai][bj][m][0], a1 = acc[ai][bj][m][1];
;                     u32x4 w; w.x = pk_bf16(h[0] * ALPHA + a0[0], h[1] * ALPHA + a0[1]); w.y = pk_bf16(h[2] * ALPHA + a0[2], h[3] * ALPHA + a0[3]);
;                     w.z = pk_bf16(h[4] * ALPHA + a1[0], h[5] * ALPHA + a1[1]); w.w = pk_bf16(h[6] * ALPHA + a1[2], h[7] * ALPHA + a1[3]);
;                     *(u32x4*)(V + ro + bj * 128) = w; } }
.LBB0_952:
	s_waitcnt vmcnt(1)
	v_pk_fma_f32 v[12:13], v[20:21], s[74:75], v[12:13] op_sel_hi:[1,0,1]
	v_pk_fma_f32 v[14:15], v[22:23], s[74:75], v[14:15] op_sel_hi:[1,0,1]
	s_waitcnt vmcnt(0)
	v_pk_fma_f32 v[8:9], v[16:17], s[74:75], v[8:9] op_sel_hi:[1,0,1]
	v_cvt_pk_bf16_f32 v12, v12, v13
	v_cvt_pk_bf16_f32 v13, v14, v15
	v_cvt_pk_bf16_f32 v14, v8, v9
	v_pk_fma_f32 v[8:9], v[18:19], s[74:75], v[10:11] op_sel_hi:[1,0,1]
	v_lshl_add_u64 v[16:17], v[30:31], 1, s[8:9]
	v_cvt_pk_bf16_f32 v15, v8, v9
	s_and_b64 vcc, exec, s[4:5]
	global_store_dwordx4 v[16:17], v[12:15], off
	s_cbranch_vccnz .LBB0_958
	global_load_dwordx4 v[12:15], v[28:29], off offset:512 nt
	global_load_dwordx4 v[8:11], v[28:29], off offset:528 nt
	s_cbranch_execnz .LBB0_955
